# attention stages 7 layer-0 items per wave (0x8800..0xbfff); top-k phase keeps 0x3000..0x37ff, input-projection phase 0x3800..0x87ff
# baseline (speedup 1.0000x reference)
;     __device__ __forceinline__ const float* x() const { return (const float*)ld(0); }
; __device__ __forceinline__ void convert_moe_items(const Ctx& a, int layer, LAS unsigned char* lds, int it0, int it1, int widx, int nw, int wave, int lane) {
;     ...
;     int it = it0 + widx;
;     if (it >= it1) return;
;     f32x4 va[8], vb[8]; CvtItem da = decode(it), db = da; bool hb = (it + nw < it1);
;     cvt_load(da, va, lane);
;     if (hb) { db = decode(it + nw); cvt_load(db, vb, lane); }
; PHASE_FN ph_win() { PH_PRO;
;     ...
;     { const int nu = S.total(), maxu = (nu + G - 1) / G, nfull = nu - (maxu - 1) * G;
;       if ((int)blockIdx.x >= nfull && nfull < G) convert_moe_items(a, 0, lds, L0_B, MOE_ITEMS, ((int)blockIdx.x - nfull) * NWAVES + wave, (G - nfull) * NWAVES, wave, lane);
;       else if (nfull >= G) { convert_moe_items(a, 0, lds, L0_B, MOE_ITEMS, gw, NGW, wave, lane); router_prep(a, G, tid, lane, wave); }
.LBB0_348:
	s_waitcnt lgkmcnt(0)
	s_abs_i32 s0, s47
	v_cvt_f32_u32_e32 v2, s0
	s_sub_i32 s3, 0, s0
	s_add_i32 s1, s47, 0x287
	s_xor_b32 s2, s1, s47
	v_rcp_iflag_f32_e32 v2, v2
	s_abs_i32 s1, s1
	s_ashr_i32 s2, s2, 31
	v_mul_f32_e32 v2, 0x4f7ffffe, v2
	v_cvt_u32_f32_e32 v2, v2
	s_nop 0
	v_readfirstlane_b32 s4, v2
	s_mul_i32 s3, s3, s4
	s_mul_hi_u32 s3, s4, s3
	s_add_i32 s4, s4, s3
	s_mul_hi_u32 s3, s1, s4
	s_mul_i32 s4, s3, s0
	s_sub_i32 s1, s1, s4
	s_add_i32 s5, s3, 1
	s_sub_i32 s4, s1, s0
	s_cmp_ge_u32 s1, s0
	s_cselect_b32 s3, s5, s3
	s_cselect_b32 s1, s4, s1
	s_add_i32 s4, s3, 1
	s_cmp_ge_u32 s1, s0
	s_cselect_b32 s0, s4, s3
	s_xor_b32 s0, s0, s2
	s_sub_i32 s28, s0, s2
	s_add_i32 s0, s28, -1
	s_mul_i32 s0, s0, s47
	s_sub_i32 s29, 0x288, s0
	s_cmp_lt_i32 s96, s29
	s_cselect_b64 s[2:3], -1, 0
	s_cmp_le_i32 s47, s29
	s_cselect_b64 s[0:1], -1, 0
	s_or_b64 s[4:5], s[2:3], s[0:1]
	s_mov_b64 s[2:3], -1
	s_and_b64 vcc, exec, s[4:5]
	s_cbranch_vccz .LBB0_423
	s_lshl_b32 s2, s96, 3
	s_andn2_b64 vcc, exec, s[0:1]
	s_add_i32 s30, s58, s2
	s_cbranch_vccnz .LBB0_354
	s_add_i32 s0, 0, 0x23f10
	v_mov_b32_e32 v2, s0
	s_add_i32 s0, 0, 0x23ee8
	v_mov_b32_e32 v4, s0
	s_add_i32 s0, 0, 0x23ef8
	s_waitcnt vmcnt(0)
	v_mov_b32_e32 v8, s0
	ds_read_b64 v[2:3], v2
	ds_read2_b64 v[4:7], v4 offset1:1
	ds_read_b64 v[8:9], v8
	s_lshl_b32 s31, s47, 3
	s_cmpk_gt_i32 s30, 0x87ff
	s_waitcnt lgkmcnt(2)
	v_readfirstlane_b32 s2, v3
	v_readfirstlane_b32 s3, v2
	s_waitcnt lgkmcnt(1)
	v_readfirstlane_b32 s33, v5
	v_readfirstlane_b32 s34, v4
	v_readfirstlane_b32 s35, v7
	v_readfirstlane_b32 s36, v6
	s_waitcnt lgkmcnt(0)
	v_readfirstlane_b32 s37, v9
	v_readfirstlane_b32 s38, v8
	s_cbranch_scc1 .LBB0_401
	s_add_u32 s0, s3, 0x2530000
	s_addc_u32 s1, s2, 0
	s_add_u32 s4, s3, 0x12530000
	s_addc_u32 s5, s2, 0
	s_add_i32 s41, s30, 0x3800
	s_mul_hi_i32 s2, s41, 0x2aaaaaab
	s_lshr_b32 s3, s2, 31
	s_ashr_i32 s2, s2, 9
	s_add_i32 s2, s2, s3
	s_mul_i32 s3, s2, 0xc00
	s_sub_i32 s13, s41, s3
	s_ashr_i32 s3, s2, 31
	s_lshl_b64 s[8:9], s[2:3], 21
	s_lshl_b32 s17, s2, 11
	s_cmpk_gt_i32 s13, 0x3ff
	s_cbranch_scc0 .LBB0_355
	s_cmpk_gt_u32 s13, 0x7ff
	s_cbranch_scc0 .LBB0_356
	s_add_i32 s16, s13, 0xfffff800
	s_lshl_b64 s[2:3], s[8:9], 2
	s_add_u32 s2, s38, s2
	s_addc_u32 s3, s37, s3
	s_mov_b64 s[6:7], 0
	s_branch .LBB0_357

; #define LAS __attribute__((address_space(3)))
;     __device__ __forceinline__ const float* x() const { return (const float*)ld(0); }
;     __device__ __forceinline__ const float* w_gate() const { return (const float*)ld(21); }
;     __device__ __forceinline__ const float* w_up() const { return (const float*)ld(22); }
;     __device__ __forceinline__ const float* w_down() const { return (const float*)ld(23); }
;     __device__ __forceinline__ unsigned char* ws() const { return (unsigned char*)ld(26); }
; __device__ __forceinline__ void convert_moe_items(const Ctx& a, int layer, LAS unsigned char* lds, int it0, int it1, int widx, int nw, int wave, int lane) {
;     LAS float* scr = (LAS float*)(lds + wave * 16384);
;     bf16_t* WGU = (bf16_t*)(a.ws() + WS_WGU + (size_t)layer * WGU_BYTES); bf16_t* WD = (bf16_t*)(a.ws() + WS_WD + (size_t)layer * WD_BYTES);
;     constexpr int I_G = (DM / 64) * (FE / 32), I_D = (FE / 64) * (DM / 32);
;     constexpr int PER_E = 2 * I_G + I_D;
;     const float *wg = a.w_gate(), *wu = a.w_up(), *wd = a.w_down();
;     auto decode = [&](int it) { CvtItem d; const int e = it / PER_E; int r = it % PER_E; const size_t eo = ((size_t)layer * NE + e) * (size_t)DM * FE;
;         if (r < I_G)          { d.src = wg + eo; d.dst = WGU; d.N = FE; d.K = DM; d.row_off = e * 2048; d.ilv = 1; }
;         else if (r < 2 * I_G) { r -= I_G; d.src = wu + eo; d.dst = WGU; d.N = FE; d.K = DM; d.row_off = e * 2048 + 128; d.ilv = 1; }
;         else                  { r -= 2 * I_G; d.src = wd + eo; d.dst = WD; d.N = DM; d.K = FE; d.row_off = e * 2048; d.ilv = 0; }
;         const int nblk = d.N / 32; d.k0 = 64 * (r / nblk); d.n0 = 32 * (r % nblk); return d; };
; PHASE_FN ph_win() { PH_PRO;
;     ...
;     { const int nu = S.total(), maxu = (nu + G - 1) / G, nfull = nu - (maxu - 1) * G;
;       if ((int)blockIdx.x >= nfull && nfull < G) convert_moe_items(a, 0, lds, L0_B, MOE_ITEMS, ((int)blockIdx.x - nfull) * NWAVES + wave, (G - nfull) * NWAVES, wave, lane);
.LBB0_423:
	s_andn2_b64 vcc, exec, s[2:3]
	s_cbranch_vccnz .LBB0_471
	s_sub_i32 s0, s96, s29
	s_lshl_b32 s2, s0, 3
	s_add_i32 s0, 0, 0x23f10
	v_mov_b32_e32 v2, s0
	s_waitcnt vmcnt(0)
	ds_read_b64 v[6:7], v2
	s_add_i32 s0, 0, 0x23ee8
	v_mov_b32_e32 v2, s0
	s_add_i32 s0, 0, 0x23ef8
	ds_read2_b64 v[2:5], v2 offset1:1
	s_waitcnt lgkmcnt(1)
	v_readfirstlane_b32 s4, v6
	v_mov_b32_e32 v6, s0
	v_readfirstlane_b32 s3, v7
	ds_read_b64 v[6:7], v6
	s_add_i32 s2, s2, s58
	s_waitcnt lgkmcnt(1)
	v_readfirstlane_b32 s30, v3
	v_readfirstlane_b32 s31, v2
	v_readfirstlane_b32 s33, v5
	v_readfirstlane_b32 s34, v4
	s_waitcnt lgkmcnt(0)
	v_readfirstlane_b32 s35, v7
	s_cmpk_gt_u32 s2, 0x4fff
	v_readfirstlane_b32 s36, v6
	s_cbranch_scc1 .LBB0_471
	s_add_u32 s0, s4, 0x2530000
	s_addc_u32 s1, s3, 0
	s_add_u32 s4, s4, 0x12530000
	s_addc_u32 s5, s3, 0
	s_add_i32 s39, s2, 0x3800
	s_and_b32 s2, s39, 0xffff
	s_mul_i32 s2, s2, 0xaaab
	s_lshr_b32 s2, s2, 27
	s_mul_i32 s3, s2, 0xc00
	s_sub_i32 s3, s39, s3
	s_and_b32 s10, s3, 0xffff
	s_lshl_b32 s16, s2, 21
	s_lshl_b32 s11, s2, 11
	s_cmpk_gt_u32 s10, 0x3ff
	s_cbranch_scc0 .LBB0_430
	s_cmpk_gt_u32 s10, 0x7ff
	s_cbranch_scc0 .LBB0_436
	s_add_i32 s13, s10, 0xfffff800
	s_lshl_b32 s2, s16, 2
	s_add_u32 s2, s36, s2
	s_addc_u32 s3, s35, 0
	s_mov_b32 s27, 1
	s_cbranch_execz .LBB0_437
	s_movk_i32 s12, 0x800
	s_movk_i32 s37, 0x400
	s_mov_b32 s27, 0
	s_mov_b32 s38, s11
	s_mov_b64 s[6:7], s[4:5]
	s_cbranch_execz .LBB0_431
	s_branch .LBB0_432

; __device__ __forceinline__ void cvt_load(const CvtItem& d, f32x4 (&v)[8], int lane) {
;     const float* p = d.src + (size_t)(d.k0 + (lane >> 3)) * d.N + d.n0 + (lane & 7) * 4;
; #pragma unroll
;     for (int q = 0; q < 8; ++q) v[q] = __builtin_nontemporal_load((const f32x4*)(p + (size_t)(8 * q) * d.N));
; }
; __device__ __forceinline__ void convert_moe_items(const Ctx& a, int layer, LAS unsigned char* lds, int it0, int it1, int widx, int nw, int wave, int lane) {
;     ...
;     int it = it0 + widx;
;     if (it >= it1) return;
;     f32x4 va[8], vb[8]; CvtItem da = decode(it), db = da; bool hb = (it + nw < it1);
;     cvt_load(da, va, lane);
;     if (hb) { db = decode(it + nw); cvt_load(db, vb, lane); }
.LBB0_432:
	s_lshr_b32 s10, s12, 5
	s_ff1_i32_b32 s8, s10
	s_lshr_b32 s8, s13, s8
	s_and_b32 s8, s8, 0xffff
	s_lshl_b32 s8, s8, 6
	v_lshrrev_b32_e32 v70, 3, v214
	s_sub_i32 s9, s47, s29
	s_add_i32 s10, s10, -1
	v_or_b32_e32 v2, s8, v70
	s_lshl_b32 s11, s9, 3
	s_and_b32 s10, s10, s13
	s_mov_b32 s13, 0
	v_mul_hi_u32_u24_e32 v3, s12, v2
	v_mul_u32_u24_e32 v2, s12, v2
	s_lshl_b32 s10, s10, 5
	s_add_i32 s18, s39, s11
	v_lshl_add_u64 v[2:3], v[2:3], 2, s[2:3]
	s_mov_b32 s11, s13
	v_and_b32_e32 v1, 28, v1
	s_cmp_lt_i32 s18, 0x8800
	v_lshl_add_u64 v[2:3], s[10:11], 2, v[2:3]
	v_mov_b32_e32 v67, 0
	v_lshlrev_b32_e32 v66, 2, v1
	s_cselect_b64 s[16:17], -1, 0
	s_lshl_b64 s[20:21], s[12:13], 5
	v_lshl_add_u64 v[10:11], v[2:3], 0, v[66:67]
	v_lshl_add_u64 v[12:13], v[10:11], 0, s[20:21]
	v_lshl_add_u64 v[18:19], v[12:13], 0, s[20:21]
	v_lshl_add_u64 v[20:21], v[18:19], 0, s[20:21]
	v_lshl_add_u64 v[26:27], v[20:21], 0, s[20:21]
	v_lshl_add_u64 v[28:29], v[26:27], 0, s[20:21]
	v_lshl_add_u64 v[34:35], v[28:29], 0, s[20:21]
	global_load_dwordx4 v[2:5], v[10:11], off nt
	global_load_dwordx4 v[6:9], v[12:13], off nt
	s_nop 0
	global_load_dwordx4 v[10:13], v[18:19], off nt
	global_load_dwordx4 v[14:17], v[20:21], off nt
	s_nop 0
	global_load_dwordx4 v[18:21], v[26:27], off nt
	global_load_dwordx4 v[22:25], v[28:29], off nt
	v_lshl_add_u64 v[36:37], v[34:35], 0, s[20:21]
	global_load_dwordx4 v[26:29], v[34:35], off nt
	global_load_dwordx4 v[30:33], v[36:37], off nt
	s_cmp_gt_i32 s18, 0x87ff
	s_mov_b64 s[12:13], s[6:7]
	s_mov_b32 s40, s37
	s_mov_b32 s41, s38
	s_mov_b32 s29, s27
	s_mov_b32 s20, s8
	s_mov_b32 s22, s10
	s_cbranch_scc1 .LBB0_447
	s_mul_hi_i32 s2, s18, 0x2aaaaaab
	s_lshr_b32 s3, s2, 31
	s_ashr_i32 s2, s2, 9
	s_add_i32 s2, s2, s3
	s_mul_i32 s3, s2, 0xc00
	s_sub_i32 s19, s18, s3
	s_ashr_i32 s3, s2, 31
	s_lshl_b64 s[20:21], s[2:3], 21
	s_lshl_b32 s24, s2, 11
	s_cmpk_gt_i32 s19, 0x3ff
	s_cbranch_scc0 .LBB0_438
	s_cmpk_gt_u32 s19, 0x7ff
	s_cbranch_scc0 .LBB0_439
	s_add_i32 s11, s19, 0xfffff800
	s_lshl_b64 s[2:3], s[20:21], 2
	s_add_u32 s2, s36, s2
	s_addc_u32 s3, s35, s3
	s_mov_b64 s[12:13], 0
	s_branch .LBB0_440

; #define LAS __attribute__((address_space(3)))
; __device__ __forceinline__ unsigned pk2(float lo, float hi) { return f2bf(lo) | (f2bf(hi) << 16); }
;     __device__ __forceinline__ const float* x() const { return (const float*)ld(0); }
;     __device__ __forceinline__ const float* c() const { return (const float*)ld(1); }
; template <bool NT = true> __device__ __forceinline__ void cvt_store(const CvtItem& d, const f32x4 (&v)[8], LAS float* scr, int lane) {
;     const int rr = lane >> 3, c4 = (lane & 7) * 4;
; #pragma unroll
;     for (int q = 0; q < 8; ++q) { LAS float* t = scr + (8 * q + rr) * 33 + c4; t[0] = v[q].x; t[1] = v[q].y; t[2] = v[q].z; t[3] = v[q].w; }
;     asm volatile("s_waitcnt lgkmcnt(0)" ::: "memory");
;     const int c = lane & 7;
; #pragma unroll
;     for (int j = 0; j < 4; ++j) { const int n = (lane >> 3) + 8 * j; const LAS float* s = scr + (8 * c) * 33 + n;
;         u32x4 o; o.x = pk2(s[0 * 33], s[1 * 33]); o.y = pk2(s[2 * 33], s[3 * 33]); o.z = pk2(s[4 * 33], s[5 * 33]); o.w = pk2(s[6 * 33], s[7 * 33]);
;         const int ng = d.n0 + n, drow = d.row_off + (d.ilv ? ((ng >> 7) * 256 + (ng & 127)) : ng);
;         if (NT) __builtin_nontemporal_store(o, (u32x4*)(d.dst + (size_t)drow * d.K + d.k0 + 8 * c)); else *(u32x4*)(d.dst + (size_t)drow * d.K + d.k0 + 8 * c) = o; }
;     asm volatile("s_waitcnt lgkmcnt(0)" ::: "memory");
; __device__ __forceinline__ void convert_moe_items(const Ctx& a, int layer, LAS unsigned char* lds, int it0, int it1, int widx, int nw, int wave, int lane) {
;     ...
;         it += 2 * nw; const bool ha = (it < it1);
;         if (ha) { da = decode(it); cvt_load(da, va, lane); }
.Lcvt_p2b_t:
	v_add_u32_e32 v79, 0x420, v74
	v_add_u32_e32 v80, 0x428, v74
	v_add_u32_e32 v81, 0x840, v74
	v_add_u32_e32 v82, 0x848, v74
	v_add_u32_e32 v83, 0xc60, v74
	v_add_u32_e32 v84, 0xc68, v74
	v_add_u32_e32 v85, 0x1080, v74
	v_add_u32_e32 v86, 0x1088, v74
	v_add_u32_e32 v87, 0x14a0, v74
	v_add_u32_e32 v88, 0x14a8, v74
	v_add_u32_e32 v89, 0x18c0, v74
	v_add_u32_e32 v90, 0x18c8, v74
	v_add_u32_e32 v91, 0x1ce0, v74
	v_add_u32_e32 v92, 0x1ce8, v74
	s_waitcnt vmcnt(15)
	ds_write2_b32 v74, v2, v3 offset1:1
	ds_write2_b32 v74, v4, v5 offset0:2 offset1:3
	s_waitcnt vmcnt(14)
	ds_write2_b32 v79, v6, v7 offset1:1
	ds_write2_b32 v80, v8, v9 offset1:1
	s_waitcnt vmcnt(13)
	ds_write2_b32 v81, v10, v11 offset1:1
	ds_write2_b32 v82, v12, v13 offset1:1
	s_waitcnt vmcnt(12)
	ds_write2_b32 v83, v14, v15 offset1:1
	ds_write2_b32 v84, v16, v17 offset1:1
	s_waitcnt vmcnt(11)
	ds_write2_b32 v85, v18, v19 offset1:1
	ds_write2_b32 v86, v20, v21 offset1:1
	s_waitcnt vmcnt(10)
	ds_write2_b32 v87, v22, v23 offset1:1
	ds_write2_b32 v88, v24, v25 offset1:1
	s_waitcnt vmcnt(9)
	ds_write2_b32 v89, v26, v27 offset1:1
	ds_write2_b32 v90, v28, v29 offset1:1
	s_waitcnt vmcnt(8)
	ds_write2_b32 v91, v30, v31 offset1:1
	ds_write2_b32 v92, v32, v33 offset1:1
	s_waitcnt lgkmcnt(0)
	ds_read2_b32 v[98:99], v73 offset1:8
	ds_read2_b32 v[100:101], v73 offset0:33 offset1:41
	ds_read2_b32 v[102:103], v73 offset0:66 offset1:74
	ds_read2_b32 v[104:105], v73 offset0:99 offset1:107
	ds_read2_b32 v[106:107], v73 offset0:132 offset1:140
	s_waitcnt lgkmcnt(4)
	v_bfe_u32 v67, v98, 16, 1
	v_add3_u32 v67, v98, v67, s43
	s_waitcnt lgkmcnt(3)
	v_bfe_u32 v93, v100, 16, 1
	v_lshrrev_b32_e32 v67, 16, v67
	v_add3_u32 v93, v100, v93, s43
	ds_read2_b32 v[108:109], v73 offset0:165 offset1:173
	v_and_or_b32 v94, v93, s44, v67
	s_waitcnt lgkmcnt(3)
	v_bfe_u32 v67, v102, 16, 1
	v_add3_u32 v67, v102, v67, s43
	s_waitcnt lgkmcnt(2)
	v_bfe_u32 v93, v104, 16, 1
	ds_read2_b32 v[110:111], v73 offset0:198 offset1:206
	v_lshrrev_b32_e32 v67, 16, v67
	v_add3_u32 v93, v104, v93, s43
	ds_read2_b32 v[112:113], v73 offset0:231 offset1:239
	v_and_or_b32 v95, v93, s44, v67
	s_waitcnt lgkmcnt(3)
	v_bfe_u32 v67, v106, 16, 1
	v_add3_u32 v67, v106, v67, s43
	s_waitcnt lgkmcnt(2)
	v_bfe_u32 v93, v108, 16, 1
	v_lshrrev_b32_e32 v67, 16, v67
	v_add3_u32 v93, v108, v93, s43
	v_and_or_b32 v96, v93, s44, v67
	s_waitcnt lgkmcnt(1)
	v_bfe_u32 v67, v110, 16, 1
	v_add3_u32 v67, v110, v67, s43
	s_waitcnt lgkmcnt(0)
	v_bfe_u32 v93, v112, 16, 1
	s_cmp_eq_u32 s27, 0
	v_lshrrev_b32_e32 v67, 16, v67
	v_add3_u32 v93, v112, v93, s43
	s_cselect_b64 vcc, -1, 0
	s_lshl_b32 s2, s10, 1
	v_and_or_b32 v97, v93, s44, v67
	s_and_b32 s11, s2, 0xffffff00
	v_bitop3_b32 v93, s10, v75, v70 bitop3:0xc8
	v_or_b32_e32 v67, s10, v70
	v_or_b32_e32 v93, s11, v93
	v_cndmask_b32_e32 v67, v93, v67, vcc
	v_add_u32_e32 v67, s38, v67
	v_mad_u64_u32 v[114:115], s[2:3], v67, s37, 0
	v_ashrrev_i32_e32 v93, 31, v67
	v_mov_b32_e32 v98, v115
	v_mad_u64_u32 v[116:117], s[2:3], v93, s37, v[98:99]
	v_mov_b32_e32 v115, v116
	s_ashr_i32 s9, s8, 31
	v_lshl_add_u64 v[114:115], v[114:115], 1, s[6:7]
	s_lshl_b64 s[2:3], s[8:9], 1
	v_bfe_u32 v67, v99, 16, 1
	v_lshl_add_u64 v[114:115], v[114:115], 0, s[2:3]
	v_add3_u32 v67, v99, v67, s43
	v_bfe_u32 v93, v101, 16, 1
	v_lshl_add_u64 v[114:115], v[114:115], 0, v[68:69]
	v_lshrrev_b32_e32 v67, 16, v67
	v_add3_u32 v93, v101, v93, s43
	global_store_dwordx4 v[114:115], v[94:97], off nt
	s_add_i32 s46, s39, s42
	s_cmp_gt_i32 s46, 0x87ff
	v_and_or_b32 v94, v93, s44, v67
	v_bfe_u32 v67, v103, 16, 1
	v_add3_u32 v67, v103, v67, s43
	v_bfe_u32 v93, v105, 16, 1
	v_lshrrev_b32_e32 v67, 16, v67
	v_add3_u32 v93, v105, v93, s43
	v_and_or_b32 v95, v93, s44, v67
	v_bfe_u32 v67, v107, 16, 1
	v_add3_u32 v67, v107, v67, s43
	v_bfe_u32 v93, v109, 16, 1
	v_lshrrev_b32_e32 v67, 16, v67
	v_add3_u32 v93, v109, v93, s43
	v_and_or_b32 v96, v93, s44, v67
	v_bfe_u32 v67, v111, 16, 1
	v_add3_u32 v67, v111, v67, s43
	v_bfe_u32 v93, v113, 16, 1
	v_lshrrev_b32_e32 v67, 16, v67
	v_add3_u32 v93, v113, v93, s43
	v_and_or_b32 v97, v93, s44, v67
	v_bitop3_b32 v93, s10, v76, v1 bitop3:0xc8
	v_or_b32_e32 v67, s10, v1
	v_or_b32_e32 v93, s11, v93
	v_cndmask_b32_e32 v67, v93, v67, vcc
	v_add_u32_e32 v67, s38, v67
	v_mad_u64_u32 v[98:99], s[24:25], v67, s37, 0
	v_ashrrev_i32_e32 v93, 31, v67
	v_mov_b32_e32 v100, v99
	v_mad_u64_u32 v[100:101], s[24:25], v93, s37, v[100:101]
	v_mov_b32_e32 v99, v100
	v_lshl_add_u64 v[98:99], v[98:99], 1, s[6:7]
	v_lshl_add_u64 v[98:99], v[98:99], 0, s[2:3]
	ds_read2_b32 v[100:101], v73 offset0:16 offset1:24
	v_lshl_add_u64 v[98:99], v[98:99], 0, v[68:69]
	global_store_dwordx4 v[98:99], v[94:97], off nt
	ds_read2_b32 v[98:99], v73 offset0:49 offset1:57
	ds_read2_b32 v[102:103], v73 offset0:82 offset1:90
	ds_read2_b32 v[104:105], v73 offset0:115 offset1:123
	s_waitcnt lgkmcnt(3)
; #define LAS __attribute__((address_space(3)))
; __device__ __forceinline__ unsigned pk2(float lo, float hi) { return f2bf(lo) | (f2bf(hi) << 16); }
;     __device__ __forceinline__ const float* x() const { return (const float*)ld(0); }
;     __device__ __forceinline__ const float* c() const { return (const float*)ld(1); }
; template <bool NT = true> __device__ __forceinline__ void cvt_store(const CvtItem& d, const f32x4 (&v)[8], LAS float* scr, int lane) {
;     ...
;     for (int j = 0; j < 4; ++j) { const int n = (lane >> 3) + 8 * j; const LAS float* s = scr + (8 * c) * 33 + n;
;         u32x4 o; o.x = pk2(s[0 * 33], s[1 * 33]); o.y = pk2(s[2 * 33], s[3 * 33]); o.z = pk2(s[4 * 33], s[5 * 33]); o.w = pk2(s[6 * 33], s[7 * 33]);
;         const int ng = d.n0 + n, drow = d.row_off + (d.ilv ? ((ng >> 7) * 256 + (ng & 127)) : ng);
;         if (NT) __builtin_nontemporal_store(o, (u32x4*)(d.dst + (size_t)drow * d.K + d.k0 + 8 * c)); else *(u32x4*)(d.dst + (size_t)drow * d.K + d.k0 + 8 * c) = o; }
;     asm volatile("s_waitcnt lgkmcnt(0)" ::: "memory");
; __device__ __forceinline__ void convert_moe_items(const Ctx& a, int layer, LAS unsigned char* lds, int it0, int it1, int widx, int nw, int wave, int lane) {
;     ...
;         it += 2 * nw; const bool ha = (it < it1);
;         if (ha) { da = decode(it); cvt_load(da, va, lane); }
;         if (!hb) break;
;         cvt_store(db, vb, scr, lane);
;         hb = (it + nw < it1);
;         if (hb) { db = decode(it + nw); cvt_load(db, vb, lane); }
	v_bfe_u32 v67, v100, 16, 1
	v_add3_u32 v67, v100, v67, s43
	s_waitcnt lgkmcnt(2)
	v_bfe_u32 v93, v98, 16, 1
	ds_read2_b32 v[106:107], v73 offset0:148 offset1:156
	v_lshrrev_b32_e32 v67, 16, v67
	v_add3_u32 v93, v98, v93, s43
	ds_read2_b32 v[108:109], v73 offset0:181 offset1:189
	v_and_or_b32 v94, v93, s44, v67
	s_waitcnt lgkmcnt(3)
	v_bfe_u32 v67, v102, 16, 1
	v_add3_u32 v67, v102, v67, s43
	s_waitcnt lgkmcnt(2)
	v_bfe_u32 v93, v104, 16, 1
	ds_read2_b32 v[110:111], v73 offset0:214 offset1:222
	v_lshrrev_b32_e32 v67, 16, v67
	v_add3_u32 v93, v104, v93, s43
	ds_read2_b32 v[112:113], v73 offset0:247 offset1:255
	v_and_or_b32 v95, v93, s44, v67
	s_waitcnt lgkmcnt(3)
	v_bfe_u32 v67, v106, 16, 1
	v_add3_u32 v67, v106, v67, s43
	s_waitcnt lgkmcnt(2)
	v_bfe_u32 v93, v108, 16, 1
	v_lshrrev_b32_e32 v67, 16, v67
	v_add3_u32 v93, v108, v93, s43
	v_and_or_b32 v96, v93, s44, v67
	s_waitcnt lgkmcnt(1)
	v_bfe_u32 v67, v110, 16, 1
	v_add3_u32 v67, v110, v67, s43
	s_waitcnt lgkmcnt(0)
	v_bfe_u32 v93, v112, 16, 1
	v_lshrrev_b32_e32 v67, 16, v67
	v_add3_u32 v93, v112, v93, s43
	v_and_or_b32 v97, v93, s44, v67
	v_bitop3_b32 v93, s10, v77, v71 bitop3:0xc8
	v_or_b32_e32 v67, s10, v71
	v_or_b32_e32 v93, s11, v93
	v_cndmask_b32_e32 v67, v93, v67, vcc
	v_add_u32_e32 v67, s38, v67
	v_mad_u64_u32 v[114:115], s[24:25], v67, s37, 0
	v_ashrrev_i32_e32 v93, 31, v67
	v_mov_b32_e32 v98, v115
	v_mad_u64_u32 v[116:117], s[24:25], v93, s37, v[98:99]
	v_mov_b32_e32 v115, v116
	v_lshl_add_u64 v[114:115], v[114:115], 1, s[6:7]
	v_bfe_u32 v67, v101, 16, 1
	v_lshl_add_u64 v[114:115], v[114:115], 0, s[2:3]
	v_add3_u32 v67, v101, v67, s43
	v_bfe_u32 v93, v99, 16, 1
	v_lshl_add_u64 v[114:115], v[114:115], 0, v[68:69]
	v_lshrrev_b32_e32 v67, 16, v67
	v_add3_u32 v93, v99, v93, s43
	global_store_dwordx4 v[114:115], v[94:97], off nt
	s_nop 1
	v_and_or_b32 v94, v93, s44, v67
	v_bfe_u32 v67, v103, 16, 1
	v_add3_u32 v67, v103, v67, s43
	v_bfe_u32 v93, v105, 16, 1
	v_lshrrev_b32_e32 v67, 16, v67
	v_add3_u32 v93, v105, v93, s43
	v_and_or_b32 v95, v93, s44, v67
	v_bfe_u32 v67, v107, 16, 1
	v_add3_u32 v67, v107, v67, s43
	v_bfe_u32 v93, v109, 16, 1
	v_lshrrev_b32_e32 v67, 16, v67
	v_add3_u32 v93, v109, v93, s43
	v_and_or_b32 v96, v93, s44, v67
	v_bfe_u32 v67, v111, 16, 1
	v_add3_u32 v67, v111, v67, s43
	v_bfe_u32 v93, v113, 16, 1
	v_lshrrev_b32_e32 v67, 16, v67
	v_add3_u32 v93, v113, v93, s43
	v_and_or_b32 v97, v93, s44, v67
	v_bitop3_b32 v93, s10, v78, v72 bitop3:0xc8
	v_or_b32_e32 v67, s10, v72
	v_or_b32_e32 v93, s11, v93
	v_cndmask_b32_e32 v67, v93, v67, vcc
	v_add_u32_e32 v67, s38, v67
	v_mad_u64_u32 v[98:99], s[24:25], v67, s37, 0
	v_ashrrev_i32_e32 v93, 31, v67
	v_mov_b32_e32 v100, v99
	v_mad_u64_u32 v[100:101], s[24:25], v93, s37, v[100:101]
	v_mov_b32_e32 v99, v100
	v_lshl_add_u64 v[98:99], v[98:99], 1, s[6:7]
	v_lshl_add_u64 v[98:99], v[98:99], 0, s[2:3]
	v_lshl_add_u64 v[98:99], v[98:99], 0, v[68:69]
	global_store_dwordx4 v[98:99], v[94:97], off nt
	s_waitcnt lgkmcnt(0)
	s_cselect_b64 s[24:25], -1, 0
	s_and_b64 vcc, exec, s[24:25]
	s_cbranch_vccnz .LBB0_460
	s_mul_hi_i32 s2, s46, 0x2aaaaaab
	s_lshr_b32 s3, s2, 31
	s_ashr_i32 s2, s2, 9
	s_add_i32 s26, s2, s3
	s_mul_i32 s2, s26, 0xfffff400
	s_ashr_i32 s27, s26, 31
	s_add_i32 s23, s46, s2
	s_lshl_b64 s[8:9], s[26:27], 21
	s_lshl_b32 s47, s26, 11
	s_cmpk_gt_i32 s23, 0x3ff
	s_mov_b64 s[10:11], -1
	s_cbranch_scc0 .LBB0_457
	s_mul_i32 s2, s26, 0xc00
	s_sub_i32 s10, s46, s2
	s_cmpk_gt_u32 s23, 0x7ff
	s_mov_b64 s[6:7], -1
	s_cbranch_scc0 .LBB0_455
	s_add_i32 s21, s10, 0xfffff800
	s_lshl_b64 s[2:3], s[8:9], 2
	s_add_u32 s2, s36, s2
	s_addc_u32 s3, s35, s3
	s_mov_b64 s[6:7], 0

; #define LAS __attribute__((address_space(3)))
; __device__ __forceinline__ unsigned pk2(float lo, float hi) { return f2bf(lo) | (f2bf(hi) << 16); }
;     __device__ __forceinline__ const float* x() const { return (const float*)ld(0); }
;     __device__ __forceinline__ const float* c() const { return (const float*)ld(1); }
; template <bool NT = true> __device__ __forceinline__ void cvt_store(const CvtItem& d, const f32x4 (&v)[8], LAS float* scr, int lane) {
;     const int rr = lane >> 3, c4 = (lane & 7) * 4;
; #pragma unroll
;     for (int q = 0; q < 8; ++q) { LAS float* t = scr + (8 * q + rr) * 33 + c4; t[0] = v[q].x; t[1] = v[q].y; t[2] = v[q].z; t[3] = v[q].w; }
;     asm volatile("s_waitcnt lgkmcnt(0)" ::: "memory");
;     const int c = lane & 7;
; #pragma unroll
;     for (int j = 0; j < 4; ++j) { const int n = (lane >> 3) + 8 * j; const LAS float* s = scr + (8 * c) * 33 + n;
;         u32x4 o; o.x = pk2(s[0 * 33], s[1 * 33]); o.y = pk2(s[2 * 33], s[3 * 33]); o.z = pk2(s[4 * 33], s[5 * 33]); o.w = pk2(s[6 * 33], s[7 * 33]);
;         const int ng = d.n0 + n, drow = d.row_off + (d.ilv ? ((ng >> 7) * 256 + (ng & 127)) : ng);
;         if (NT) __builtin_nontemporal_store(o, (u32x4*)(d.dst + (size_t)drow * d.K + d.k0 + 8 * c)); else *(u32x4*)(d.dst + (size_t)drow * d.K + d.k0 + 8 * c) = o; }
;     asm volatile("s_waitcnt lgkmcnt(0)" ::: "memory");
.Lcvt_p2b_m:
	s_waitcnt vmcnt(12)
	ds_write2_b32 v74, v34, v35 offset1:1
	ds_write2_b32 v74, v36, v37 offset0:2 offset1:3
	ds_write2_b32 v79, v38, v39 offset1:1
	ds_write2_b32 v80, v40, v41 offset1:1
	ds_write2_b32 v81, v42, v43 offset1:1
	ds_write2_b32 v82, v44, v45 offset1:1
	ds_write2_b32 v83, v46, v47 offset1:1
	ds_write2_b32 v84, v48, v49 offset1:1
	ds_write2_b32 v85, v50, v51 offset1:1
	ds_write2_b32 v86, v52, v53 offset1:1
	ds_write2_b32 v87, v54, v55 offset1:1
	ds_write2_b32 v88, v56, v57 offset1:1
	ds_write2_b32 v89, v58, v59 offset1:1
	ds_write2_b32 v90, v60, v61 offset1:1
	ds_write2_b32 v91, v62, v63 offset1:1
	ds_write2_b32 v92, v64, v65 offset1:1
	s_waitcnt lgkmcnt(0)
	ds_read2_b32 v[84:85], v73 offset1:8
	ds_read2_b32 v[86:87], v73 offset0:33 offset1:41
	ds_read2_b32 v[88:89], v73 offset0:66 offset1:74
	ds_read2_b32 v[90:91], v73 offset0:99 offset1:107
	ds_read2_b32 v[92:93], v73 offset0:132 offset1:140
	s_waitcnt lgkmcnt(4)
	v_bfe_u32 v67, v84, 16, 1
	v_add3_u32 v67, v84, v67, s43
	s_waitcnt lgkmcnt(3)
	v_bfe_u32 v79, v86, 16, 1
	v_lshrrev_b32_e32 v67, 16, v67
	v_add3_u32 v79, v86, v79, s43
	ds_read2_b32 v[94:95], v73 offset0:165 offset1:173
	v_and_or_b32 v80, v79, s44, v67
	s_waitcnt lgkmcnt(3)
	v_bfe_u32 v67, v88, 16, 1
	v_add3_u32 v67, v88, v67, s43
	s_waitcnt lgkmcnt(2)
	v_bfe_u32 v79, v90, 16, 1
	ds_read2_b32 v[96:97], v73 offset0:198 offset1:206
	v_lshrrev_b32_e32 v67, 16, v67
	v_add3_u32 v79, v90, v79, s43
	ds_read2_b32 v[98:99], v73 offset0:231 offset1:239
	v_and_or_b32 v81, v79, s44, v67
	s_waitcnt lgkmcnt(3)
	v_bfe_u32 v67, v92, 16, 1
	v_add3_u32 v67, v92, v67, s43
	s_waitcnt lgkmcnt(2)
	v_bfe_u32 v79, v94, 16, 1
	v_lshrrev_b32_e32 v67, 16, v67
	v_add3_u32 v79, v94, v79, s43
	v_and_or_b32 v82, v79, s44, v67
	s_waitcnt lgkmcnt(1)
	v_bfe_u32 v67, v96, 16, 1
	v_add3_u32 v67, v96, v67, s43
	s_waitcnt lgkmcnt(0)
	v_bfe_u32 v79, v98, 16, 1
	v_lshrrev_b32_e32 v67, 16, v67
	v_add3_u32 v79, v98, v79, s43
	v_and_or_b32 v83, v79, s44, v67
	v_add_u32_e32 v67, s22, v70
	s_cmp_eq_u32 s29, 0
	v_lshlrev_b32_e32 v79, 1, v67
	v_and_b32_e32 v84, 0x7f, v67
	v_and_or_b32 v79, v79, s45, v84
	s_cselect_b64 vcc, -1, 0
	v_cndmask_b32_e32 v67, v79, v67, vcc
	v_add_u32_e32 v67, s41, v67
	v_mad_u64_u32 v[100:101], s[2:3], v67, s40, 0
	v_ashrrev_i32_e32 v79, 31, v67
	v_mov_b32_e32 v84, v101
	v_mad_u64_u32 v[102:103], s[2:3], v79, s40, v[84:85]
	v_mov_b32_e32 v101, v102
	s_ashr_i32 s21, s20, 31
	v_lshl_add_u64 v[100:101], v[100:101], 1, s[12:13]
	s_lshl_b64 s[2:3], s[20:21], 1
	v_bfe_u32 v67, v85, 16, 1
	v_lshl_add_u64 v[100:101], v[100:101], 0, s[2:3]
	v_add3_u32 v67, v85, v67, s43
	v_bfe_u32 v79, v87, 16, 1
	v_lshl_add_u64 v[100:101], v[100:101], 0, v[68:69]
	v_lshrrev_b32_e32 v67, 16, v67
	v_add3_u32 v79, v87, v79, s43
	global_store_dwordx4 v[100:101], v[80:83], off nt
	s_nop 1
	v_and_or_b32 v80, v79, s44, v67
	v_bfe_u32 v67, v89, 16, 1
	v_add3_u32 v67, v89, v67, s43
	v_bfe_u32 v79, v91, 16, 1
	v_lshrrev_b32_e32 v67, 16, v67
	v_add3_u32 v79, v91, v79, s43
	v_and_or_b32 v81, v79, s44, v67
	v_bfe_u32 v67, v93, 16, 1
	v_add3_u32 v67, v93, v67, s43
	v_bfe_u32 v79, v95, 16, 1
	v_lshrrev_b32_e32 v67, 16, v67
	v_add3_u32 v79, v95, v79, s43
	v_and_or_b32 v82, v79, s44, v67
	v_bfe_u32 v67, v97, 16, 1
	v_add3_u32 v67, v97, v67, s43
	v_bfe_u32 v79, v99, 16, 1
	v_lshrrev_b32_e32 v67, 16, v67
	v_add3_u32 v79, v99, v79, s43
	v_and_or_b32 v83, v79, s44, v67
	v_add_u32_e32 v67, s22, v1
	v_lshlrev_b32_e32 v79, 1, v67
	v_and_b32_e32 v84, 0x7f, v67
	v_and_or_b32 v79, v79, s45, v84
	v_cndmask_b32_e32 v67, v79, v67, vcc
	v_add_u32_e32 v67, s41, v67
	v_mad_u64_u32 v[84:85], s[16:17], v67, s40, 0
	v_ashrrev_i32_e32 v79, 31, v67
	v_mov_b32_e32 v86, v85
	v_mad_u64_u32 v[86:87], s[16:17], v79, s40, v[86:87]
	v_mov_b32_e32 v85, v86
	v_lshl_add_u64 v[84:85], v[84:85], 1, s[12:13]
	v_lshl_add_u64 v[84:85], v[84:85], 0, s[2:3]
	ds_read2_b32 v[86:87], v73 offset0:16 offset1:24
	v_lshl_add_u64 v[84:85], v[84:85], 0, v[68:69]
	global_store_dwordx4 v[84:85], v[80:83], off nt
	ds_read2_b32 v[84:85], v73 offset0:49 offset1:57
	ds_read2_b32 v[88:89], v73 offset0:82 offset1:90
	ds_read2_b32 v[90:91], v73 offset0:115 offset1:123
	s_waitcnt lgkmcnt(3)
; #define LAS __attribute__((address_space(3)))
; __device__ __forceinline__ unsigned pk2(float lo, float hi) { return f2bf(lo) | (f2bf(hi) << 16); }
;     __device__ __forceinline__ const float* x() const { return (const float*)ld(0); }
;     __device__ __forceinline__ const float* c() const { return (const float*)ld(1); }
; template <bool NT = true> __device__ __forceinline__ void cvt_store(const CvtItem& d, const f32x4 (&v)[8], LAS float* scr, int lane) {
;     ...
;     for (int j = 0; j < 4; ++j) { const int n = (lane >> 3) + 8 * j; const LAS float* s = scr + (8 * c) * 33 + n;
;         u32x4 o; o.x = pk2(s[0 * 33], s[1 * 33]); o.y = pk2(s[2 * 33], s[3 * 33]); o.z = pk2(s[4 * 33], s[5 * 33]); o.w = pk2(s[6 * 33], s[7 * 33]);
;         const int ng = d.n0 + n, drow = d.row_off + (d.ilv ? ((ng >> 7) * 256 + (ng & 127)) : ng);
;         if (NT) __builtin_nontemporal_store(o, (u32x4*)(d.dst + (size_t)drow * d.K + d.k0 + 8 * c)); else *(u32x4*)(d.dst + (size_t)drow * d.K + d.k0 + 8 * c) = o; }
;     asm volatile("s_waitcnt lgkmcnt(0)" ::: "memory");
; __device__ __forceinline__ void convert_moe_items(const Ctx& a, int layer, LAS unsigned char* lds, int it0, int it1, int widx, int nw, int wave, int lane) {
;     ...
;         cvt_store(db, vb, scr, lane);
;         hb = (it + nw < it1);
;         if (hb) { db = decode(it + nw); cvt_load(db, vb, lane); }
;         if (!ha) break;
	v_bfe_u32 v67, v86, 16, 1
	v_add3_u32 v67, v86, v67, s43
	s_waitcnt lgkmcnt(2)
	v_bfe_u32 v79, v84, 16, 1
	ds_read2_b32 v[92:93], v73 offset0:148 offset1:156
	v_lshrrev_b32_e32 v67, 16, v67
	v_add3_u32 v79, v84, v79, s43
	ds_read2_b32 v[94:95], v73 offset0:181 offset1:189
	v_and_or_b32 v80, v79, s44, v67
	s_waitcnt lgkmcnt(3)
	v_bfe_u32 v67, v88, 16, 1
	v_add3_u32 v67, v88, v67, s43
	s_waitcnt lgkmcnt(2)
	v_bfe_u32 v79, v90, 16, 1
	ds_read2_b32 v[96:97], v73 offset0:214 offset1:222
	v_lshrrev_b32_e32 v67, 16, v67
	v_add3_u32 v79, v90, v79, s43
	ds_read2_b32 v[98:99], v73 offset0:247 offset1:255
	v_and_or_b32 v81, v79, s44, v67
	s_waitcnt lgkmcnt(3)
	v_bfe_u32 v67, v92, 16, 1
	v_add3_u32 v67, v92, v67, s43
	s_waitcnt lgkmcnt(2)
	v_bfe_u32 v79, v94, 16, 1
	v_lshrrev_b32_e32 v67, 16, v67
	v_add3_u32 v79, v94, v79, s43
	v_and_or_b32 v82, v79, s44, v67
	s_waitcnt lgkmcnt(1)
	v_bfe_u32 v67, v96, 16, 1
	v_add3_u32 v67, v96, v67, s43
	s_waitcnt lgkmcnt(0)
	v_bfe_u32 v79, v98, 16, 1
	v_lshrrev_b32_e32 v67, 16, v67
	v_add3_u32 v79, v98, v79, s43
	v_and_or_b32 v83, v79, s44, v67
	v_add_u32_e32 v67, s22, v71
	v_lshlrev_b32_e32 v79, 1, v67
	v_and_b32_e32 v84, 0x7f, v67
	v_and_or_b32 v79, v79, s45, v84
	v_cndmask_b32_e32 v67, v79, v67, vcc
	v_add_u32_e32 v67, s41, v67
	v_mad_u64_u32 v[100:101], s[16:17], v67, s40, 0
	v_ashrrev_i32_e32 v79, 31, v67
	v_mov_b32_e32 v84, v101
	v_mad_u64_u32 v[102:103], s[16:17], v79, s40, v[84:85]
	v_mov_b32_e32 v101, v102
	v_lshl_add_u64 v[100:101], v[100:101], 1, s[12:13]
	v_bfe_u32 v67, v87, 16, 1
	v_lshl_add_u64 v[100:101], v[100:101], 0, s[2:3]
	v_add3_u32 v67, v87, v67, s43
	v_bfe_u32 v79, v85, 16, 1
	v_lshl_add_u64 v[100:101], v[100:101], 0, v[68:69]
	v_lshrrev_b32_e32 v67, 16, v67
	v_add3_u32 v79, v85, v79, s43
	global_store_dwordx4 v[100:101], v[80:83], off nt
	s_nop 1
	v_and_or_b32 v80, v79, s44, v67
	v_bfe_u32 v67, v89, 16, 1
	v_add3_u32 v67, v89, v67, s43
	v_bfe_u32 v79, v91, 16, 1
	v_lshrrev_b32_e32 v67, 16, v67
	v_add3_u32 v79, v91, v79, s43
	v_and_or_b32 v81, v79, s44, v67
	v_bfe_u32 v67, v93, 16, 1
	v_add3_u32 v67, v93, v67, s43
	v_bfe_u32 v79, v95, 16, 1
	v_lshrrev_b32_e32 v67, 16, v67
	v_add3_u32 v79, v95, v79, s43
	v_and_or_b32 v82, v79, s44, v67
	v_bfe_u32 v67, v97, 16, 1
	v_add3_u32 v67, v97, v67, s43
	v_bfe_u32 v79, v99, 16, 1
	v_lshrrev_b32_e32 v67, 16, v67
	v_add3_u32 v79, v99, v79, s43
	v_and_or_b32 v83, v79, s44, v67
	v_add_u32_e32 v67, s22, v72
	v_lshlrev_b32_e32 v79, 1, v67
	v_and_b32_e32 v84, 0x7f, v67
	v_and_or_b32 v79, v79, s45, v84
	v_cndmask_b32_e32 v67, v79, v67, vcc
	v_add_u32_e32 v67, s41, v67
	v_mad_u64_u32 v[84:85], s[16:17], v67, s40, 0
	v_ashrrev_i32_e32 v79, 31, v67
	v_mov_b32_e32 v86, v85
	v_mad_u64_u32 v[86:87], s[16:17], v79, s40, v[86:87]
	v_mov_b32_e32 v85, v86
	v_lshl_add_u64 v[84:85], v[84:85], 1, s[12:13]
	v_lshl_add_u64 v[84:85], v[84:85], 0, s[2:3]
	v_lshl_add_u64 v[84:85], v[84:85], 0, v[68:69]
	global_store_dwordx4 v[84:85], v[80:83], off nt
	s_add_i32 s2, s28, s39
	s_addk_i32 s2, 0xebc0
	s_waitcnt lgkmcnt(0)
	s_cmp_lt_i32 s2, 0x8800
	s_cselect_b64 s[16:17], -1, 0
	s_cmp_gt_i32 s2, 0x87ff
	s_cbranch_scc1 .LBB0_449
	s_mul_hi_i32 s3, s2, 0x2aaaaaab
	s_lshr_b32 s9, s3, 31
	s_ashr_i32 s3, s3, 9
	s_add_i32 s12, s3, s9
	s_mul_i32 s3, s12, 0xc00
	s_ashr_i32 s13, s12, 31
	s_sub_i32 s11, s2, s3
	s_lshl_b64 s[20:21], s[12:13], 21
	s_lshl_b32 s26, s12, 11
	s_cmpk_gt_i32 s11, 0x3ff
	s_mov_b64 s[22:23], -1
	s_cbranch_scc0 .LBB0_467
	s_cmpk_gt_u32 s11, 0x7ff
	s_mov_b64 s[12:13], -1
	s_cbranch_scc0 .LBB0_465
	s_add_i32 s9, s11, 0xfffff800
	s_lshl_b64 s[2:3], s[20:21], 2
	s_add_u32 s2, s36, s2
	s_addc_u32 s3, s35, s3
	s_mov_b64 s[12:13], 0

; #define LAS __attribute__((address_space(3)))
; #define WAIT_BAR(N) asm volatile("s_waitcnt vmcnt(" #N ") lgkmcnt(0)\n\ts_barrier" ::: "memory")
; #define DMA_K(t, slot) do { const bf16_t* sb_ = Kh + (long)(t) * KVBLK * DMK; glds16<0>(sb_, kvoff, (unsigned)__builtin_amdgcn_readfirstlane(kdst + (slot))); glds16<0>(sb_ + 64, kvoff, (unsigned)__builtin_amdgcn_readfirstlane(kdst + 8192 + (slot))); } while (0)
; template <int THRL> ...
;     ...
;   const bf16_t* Qw = Q + (size_t)(CTXL + qb * 128 + wq * QBLK) * DMK + head * 128 + comp * 64;
;   const bf16_t* Kh = K + head * 128; const bf16_t* Vh = V + head * 128;
;   const unsigned lds0 = (unsigned)(uintptr_t)shm;
;   LAS float* wsf = (LAS float*)(shm + LDS_WS) + wid * 64;
;   const unsigned kvoff = (unsigned)(lane * DMK + wid * 8) * 2u;
;   const unsigned vvoff = (unsigned)((16 * (wid & 3) + (lane >> 2)) * DMK + (wid >> 2) * 32 + (lane & 3) * 8) * 2u;
;   const unsigned kdst = lds0 + LDS_K + wid * 1024, vdst = lds0 + LDS_V + wid * 1024;
;     ...
;   const int vb0 = (int)(lds0 + LDS_V) + ((lane >> 4) & 1) * 32 + (lane & 3) * 8 + (4 * hi + ((lane & 15) >> 2)) * 64;
;   bf16x8 kf[8];
;   const lds_cptr shm3 = (lds_cptr)shm; const lds_cptr kp0 = shm3 + LDS_K + comp * 8192 + hi * 1024 + r32 * 16;
;   const lds_cptr vp0 = shm3 + LDS_V + ((lane >> 4) & 1) * 32 + (lane & 3) * 8 + (4 * hi + ((lane & 15) >> 2)) * 64;
;   DMA_K(0, 0); DMA_V(0, 0); DMA_K(1, SLOTB);
;   bf16x8 qr[4];
; #pragma unroll
;   for (int d0 = 0; d0 < 4; ++d0) qr[d0] = *reinterpret_cast<const bf16x8*>(&Qw[(long)r32 * DMK + d0 * 16 + hi * 8]);
;   float mhat = 0.f, l_reg = 0.f; f32x16 o[4]; o[0] = f32x16{}; o[1] = f32x16{}; o[2] = f32x16{}; o[3] = f32x16{}; f32x16 negm = f32x16{}; asm volatile("" : "+v"(negm));
;   bool resc = false;
;     ...
;   f32x16 pA0, pA1, pB0, pB1;
;   int sl_prev = 0, sl_cur = 0, sl_next = SLOTB;
;     ...
;   DMA_K(2, 2 * SLOTB);
;   WAIT_BAR(6);
;   qkt(pA0, pA1, kp0, qr, negm); asm volatile("s_nop 15\n\ts_nop 7" : "+v"(pA0), "+v"(pA1));
;   const lds_cptr qp = shm3 + LDS_Q + wid * 4096 + lane * 16;
; #pragma unroll
;   for (int d0 = 0; d0 < 4; ++d0) *(LAS bf16x8*)(shm + LDS_Q + wid * 4096 + lane * 16 + d0 * 1024) = qr[d0];
;   START(pA0, pA1);
.LBB0_527:
	s_lshl_b32 s0, s28, 1
	s_and_b32 s0, s0, 0x700
	s_add_u32 s33, s26, s0
	s_addc_u32 s53, s27, 0
	s_bfe_u32 s41, s39, 0x20006
	s_lshl_b32 s0, s36, 4
	s_and_b32 s37, s0, 0xffffff80
	s_lshl_b32 s0, s41, 5
	s_or_b32 s0, s37, s0
	s_addk_i32 s0, 0x100
	s_ashr_i32 s1, s0, 31
	s_lshr_b32 s40, s39, 6
	s_lshr_b32 s42, s39, 8
	s_lshl_b64 s[0:1], s[0:1], 11
	s_add_u32 s0, s5, s0
	s_addc_u32 s1, s17, s1
	s_lshl_b32 s2, s36, 7
	s_and_b32 s14, s2, 0x380
	s_lshl_b32 s8, s14, 1
	s_add_u32 s0, s0, s8
	s_addc_u32 s1, s1, 0
	s_lshl_b32 s43, s42, 6
	s_lshl_b32 s2, s42, 7
	s_add_u32 s2, s0, s2
	s_addc_u32 s3, s1, 0
	s_add_u32 s20, s22, s8
	s_addc_u32 s21, s23, 0
	s_add_u32 s8, s24, s8
	s_addc_u32 s9, s25, 0
	s_lshl_b32 s0, s41, 15
	s_add_i32 s0, s0, s43
	v_add_u32_e32 v235, s0, v219
	s_lshl_b32 s0, s40, 10
	s_add_i32 s49, s0, 0
	s_and_b32 s1, s39, 0x3fffffc0
	s_lshl_b32 s38, s40, 4
	s_add_i32 s46, s49, 0xc000
	s_add_u32 s44, s20, 0x80
	v_add_u32_e32 v237, s38, v218
	s_mov_b32 s0, m0
	s_mov_b32 m0, s49
	s_nop 0
	global_load_lds_dwordx4 v237, s[20:21] offset:0
	s_mov_b32 m0, s0
	s_addc_u32 s45, s21, 0
	s_add_i32 s54, s49, 0x2000
	s_mov_b32 s0, m0
	s_mov_b32 m0, s54
	s_nop 0
	global_load_lds_dwordx4 v237, s[44:45] offset:0
	s_mov_b32 m0, s0
	s_add_u32 s50, s8, 0x80
	s_mov_b32 s0, m0
	s_mov_b32 m0, s46
	s_nop 0
	global_load_lds_dwordx4 v235, s[8:9] offset:0
	s_mov_b32 m0, s0
	s_addc_u32 s51, s9, 0
	s_add_i32 s45, s49, 0xe000
	s_mov_b32 s0, m0
	s_mov_b32 m0, s45
	s_nop 0
	global_load_lds_dwordx4 v235, s[50:51] offset:0
	s_mov_b32 m0, s0
	s_add_u32 s50, s20, 0x20000
	s_addc_u32 s51, s21, 0
	s_add_i32 s52, s49, 0x4000
	s_mov_b32 s0, m0
	s_mov_b32 m0, s52
	s_nop 0
	global_load_lds_dwordx4 v237, s[50:51] offset:0
	s_mov_b32 m0, s0
	s_add_u32 s56, s20, 0x20080
	s_addc_u32 s57, s21, 0
	s_add_i32 s51, s49, 0x6000
	s_mov_b32 s0, m0
	s_mov_b32 m0, s51
	s_nop 0
	global_load_lds_dwordx4 v237, s[56:57] offset:0
	s_mov_b32 m0, s0
	global_load_dwordx4 v[66:69], v229, s[2:3]
	global_load_dwordx4 v[70:73], v229, s[2:3] offset:32
	global_load_dwordx4 v[74:77], v229, s[2:3] offset:64
	global_load_dwordx4 v[78:81], v229, s[2:3] offset:96
	v_mov_b64_e32 v[48:49], v[32:33]
	s_add_u32 s2, s20, 0x40000
	v_mov_b64_e32 v[46:47], v[30:31]
	v_mov_b64_e32 v[44:45], v[28:29]
	v_mov_b64_e32 v[42:43], v[26:27]
	v_mov_b64_e32 v[40:41], v[24:25]
	v_mov_b64_e32 v[38:39], v[22:23]
	v_mov_b64_e32 v[36:37], v[20:21]
	v_mov_b64_e32 v[34:35], v[18:19]
	s_addc_u32 s3, s21, 0
	s_add_i32 s48, s49, 0x8000
	s_mov_b32 s0, m0
	s_mov_b32 m0, s48
	s_nop 0
	global_load_lds_dwordx4 v237, s[2:3] offset:0
	s_mov_b32 m0, s0
	s_add_u32 s2, s20, 0x40080
	s_addc_u32 s3, s21, 0
	s_add_i32 s47, s49, 0xa000
	s_mov_b32 s0, m0
	s_mov_b32 m0, s47
	s_nop 0
	global_load_lds_dwordx4 v237, s[2:3] offset:0
	s_mov_b32 m0, s0
	v_lshl_add_u32 v236, s42, 13, v221
	s_waitcnt vmcnt(6) lgkmcnt(0)
	s_barrier
	ds_read_b128 v[4:7], v236
	s_lshl_b32 s2, s40, 12
	v_add_u32_e32 v233, s2, v222
	s_lshl_b32 s1, s1, 2
	s_add_i32 s50, s1, 0
	s_add_i32 s50, s50, 0x18000
	s_add_u32 s2, s20, 0x60000
	s_addc_u32 s3, s21, 0
	v_mov_b32_e32 v3, v2
	v_mov_b32_e32 v12, v2
	v_mov_b32_e32 v13, v2
	s_movk_i32 s57, 0x4000
	s_mov_b32 s0, 0
	s_mov_b32 s55, 0x8000
	v_lshl_add_u32 v232, v217, 2, s50
	v_mov_b32_e32 v238, 0
	s_mov_b32 s56, -1
	s_waitcnt vmcnt(3) lgkmcnt(0)
	v_mfma_f32_32x32x16_bf16 v[50:65], v[4:7], v[66:69], v[34:49]
	ds_read_b128 v[4:7], v236 offset:512
	s_waitcnt lgkmcnt(0)
	v_mfma_f32_32x32x16_bf16 v[34:49], v[4:7], v[66:69], v[34:49]
	ds_read_b128 v[4:7], v236 offset:2048
	s_waitcnt vmcnt(2) lgkmcnt(0)
	v_mfma_f32_32x32x16_bf16 v[50:65], v[4:7], v[70:73], v[50:65]
	ds_read_b128 v[4:7], v236 offset:2560
	s_waitcnt lgkmcnt(0)
	v_mfma_f32_32x32x16_bf16 v[34:49], v[4:7], v[70:73], v[34:49]
	ds_read_b128 v[4:7], v236 offset:4096
	ds_read_b128 v[8:11], v236 offset:4608
	ds_read_b128 v[82:85], v236 offset:6656
	ds_read_b128 v[14:17], v236 offset:6144
	s_waitcnt vmcnt(1) lgkmcnt(3)
	v_mfma_f32_32x32x16_bf16 v[50:65], v[4:7], v[74:77], v[50:65]
	v_mov_b32_e32 v4, v2
	v_mov_b32_e32 v5, v2
	v_mov_b32_e32 v6, v2
	v_mov_b32_e32 v7, v2
	s_waitcnt lgkmcnt(2)
	v_mfma_f32_32x32x16_bf16 v[34:49], v[8:11], v[74:77], v[34:49]
	v_mov_b32_e32 v8, v2
	v_mov_b32_e32 v9, v2
	v_mov_b32_e32 v10, v2
	v_mov_b32_e32 v11, v2
	s_waitcnt vmcnt(0) lgkmcnt(0)
	v_mfma_f32_32x32x16_bf16 v[50:65], v[14:17], v[78:81], v[50:65]
	v_mov_b32_e32 v16, v2
	v_mov_b32_e32 v17, v2
	v_mov_b32_e32 v14, v2
	v_mov_b32_e32 v15, v2
	v_mfma_f32_32x32x16_bf16 v[34:49], v[82:85], v[78:81], v[34:49]
	s_nop 15
	s_nop 7
	ds_write_b128 v233, v[66:69]
	ds_write_b128 v233, v[70:73] offset:1024
	ds_write_b128 v233, v[74:77] offset:2048
	ds_write_b128 v233, v[78:81] offset:3072
	v_max3_f32 v66, v50, v51, v34
	v_max3_f32 v67, v52, v53, v35
	v_mov_b64_e32 v[96:97], v[16:17]
	v_max3_f32 v66, v66, v36, v37
	v_max3_f32 v67, v67, v56, v57
	v_mov_b64_e32 v[94:95], v[14:15]
	v_max3_f32 v66, v66, v54, v55
	v_max3_f32 v67, v67, v40, v41
	v_mov_b64_e32 v[92:93], v[12:13]
	v_max3_f32 v66, v66, v38, v39
	v_max3_f32 v67, v67, v60, v61
	v_mov_b64_e32 v[90:91], v[10:11]
	v_max3_f32 v66, v66, v58, v59
	v_max3_f32 v67, v67, v44, v45
	v_mov_b64_e32 v[88:89], v[8:9]
	v_max3_f32 v66, v66, v42, v43
	v_max3_f32 v67, v67, v64, v65
	v_mov_b64_e32 v[86:87], v[6:7]
	v_max3_f32 v66, v66, v62, v63
	v_max3_f32 v67, v67, v48, v49
	v_mov_b64_e32 v[84:85], v[4:5]
	v_max3_f32 v66, v66, v46, v47
	v_mov_b64_e32 v[82:83], v[2:3]
	v_max_f32_e32 v66, v66, v67
	s_nop 0
	v_mov_b32_e32 v67, v66
	s_nop 1
	v_permlane32_swap_b32_e32 v66, v67
	v_max_f32_e32 v66, v66, v67
	s_nop 0
	v_add_f32_e32 v234, v2, v66
	v_sub_f32_e32 v50, v50, v66
	v_sub_f32_e32 v34, v34, v66
	v_sub_f32_e32 v51, v51, v66
	v_sub_f32_e32 v35, v35, v66
	v_sub_f32_e32 v52, v52, v66
	s_nop 0
	v_xor_b32_e32 v98, 0x80000000, v234
	v_mov_b32_e32 v99, v98
	v_mov_b32_e32 v100, v98
	v_mov_b32_e32 v101, v98
	v_mov_b32_e32 v102, v98
	v_mov_b32_e32 v103, v98
	v_mov_b32_e32 v104, v98
	v_mov_b32_e32 v105, v98
	v_mov_b32_e32 v106, v98
	v_mov_b32_e32 v107, v98
	v_mov_b32_e32 v108, v98
	v_mov_b32_e32 v109, v98
	v_mov_b32_e32 v110, v98
	v_mov_b32_e32 v111, v98
	v_mov_b32_e32 v112, v98
	v_mov_b32_e32 v113, v98
	s_waitcnt vmcnt(0) lgkmcnt(0)
	s_barrier
; #define WAIT_BAR(N) asm volatile("s_waitcnt vmcnt(" #N ") lgkmcnt(0)\n\ts_barrier" ::: "memory")
; #define DMA_K(t, slot) do { const bf16_t* sb_ = Kh + (long)(t) * KVBLK * DMK; glds16<0>(sb_, kvoff, (unsigned)__builtin_amdgcn_readfirstlane(kdst + (slot))); glds16<0>(sb_ + 64, kvoff, (unsigned)__builtin_amdgcn_readfirstlane(kdst + 8192 + (slot))); } while (0)
; #define DMA_V(t, slot) do { const bf16_t* sb_ = Vh + (long)(t) * KVBLK * DMK; glds16<0>(sb_, vvoff, (unsigned)__builtin_amdgcn_readfirstlane(vdst + (slot))); glds16<0>(sb_ + 64, vvoff, (unsigned)__builtin_amdgcn_readfirstlane(vdst + 8192 + (slot))); } while (0)
; #define ROT() do { sl_prev = sl_cur; sl_cur = sl_next; sl_next = (sl_next == (NSLOT - 1) * SLOTB) ? 0 : sl_next + SLOTB; } while (0)
; template <int THRL> ...
;     ...
;   START(pA0, pA1);
; #pragma unroll
;   for (int r = 0; r < 16; ++r) pA1[r] = __builtin_amdgcn_exp2f(pA1[r]);
;   WAIT_BAR(0);
;   DMA_K(3, 0); DMA_V(1, SLOTB);
;   ROT();
;   kload8(kf, kp0 + sl_cur);
;   WAIT_BAR(4);
;   s16x4 vlo[4], vhi[4]; u32x4 pw0, pw1, pw2, pw3;
	s_mov_b32 s1, m0
	s_mov_b32 m0, s49
	s_nop 0
	global_load_lds_dwordx4 v237, s[2:3] offset:0
	s_mov_b32 m0, s1
	s_add_u32 s2, s20, 0x60080
	s_addc_u32 s3, s21, 0
	s_mov_b32 s1, m0
	s_mov_b32 m0, s54
	s_nop 0
	global_load_lds_dwordx4 v237, s[2:3] offset:0
	s_mov_b32 m0, s1
	s_add_u32 s2, s8, 0x20000
	s_addc_u32 s3, s9, 0
	s_add_i32 s44, s49, 0x10000
	s_mov_b32 s1, m0
	s_mov_b32 m0, s44
	s_nop 0
	global_load_lds_dwordx4 v235, s[2:3] offset:0
	s_mov_b32 m0, s1
	s_add_u32 s2, s8, 0x20080
	s_addc_u32 s3, s9, 0
	s_add_i32 s43, s49, 0x12000
	s_mov_b32 s1, m0
	s_mov_b32 m0, s43
	s_nop 0
	global_load_lds_dwordx4 v235, s[2:3] offset:0
	s_mov_b32 m0, s1
	ds_read_b128 v[146:149], v236 offset:16384
	ds_read_b128 v[202:205], v236 offset:16896
	ds_read_b128 v[206:209], v236 offset:18432
	ds_read_b128 v[190:193], v236 offset:18944
	ds_read_b128 v[198:201], v236 offset:20480
	ds_read_b128 v[186:189], v236 offset:20992
	ds_read_b128 v[182:185], v236 offset:22528
	ds_read_b128 v[178:181], v236 offset:23040
	v_sub_f32_e32 v36, v36, v66
	v_sub_f32_e32 v53, v53, v66
	v_sub_f32_e32 v37, v37, v66
	v_sub_f32_e32 v54, v54, v66
	v_sub_f32_e32 v38, v38, v66
	v_sub_f32_e32 v55, v55, v66
	v_sub_f32_e32 v39, v39, v66
	v_sub_f32_e32 v56, v56, v66
	v_sub_f32_e32 v40, v40, v66
	v_sub_f32_e32 v57, v57, v66
	v_sub_f32_e32 v41, v41, v66
	v_sub_f32_e32 v58, v58, v66
	v_sub_f32_e32 v42, v42, v66
	v_sub_f32_e32 v59, v59, v66
	v_sub_f32_e32 v43, v43, v66
	v_sub_f32_e32 v60, v60, v66
	v_sub_f32_e32 v44, v44, v66
	v_sub_f32_e32 v61, v61, v66
	v_sub_f32_e32 v45, v45, v66
	v_sub_f32_e32 v62, v62, v66
	v_sub_f32_e32 v46, v46, v66
	v_sub_f32_e32 v63, v63, v66
	v_sub_f32_e32 v47, v47, v66
	v_sub_f32_e32 v64, v64, v66
	v_sub_f32_e32 v48, v48, v66
	v_sub_f32_e32 v65, v65, v66
	v_sub_f32_e32 v49, v49, v66
	v_exp_f32_e32 v130, v50
	v_exp_f32_e32 v131, v51
	v_exp_f32_e32 v132, v52
	v_exp_f32_e32 v133, v53
	v_exp_f32_e32 v134, v54
	v_exp_f32_e32 v135, v55
	v_exp_f32_e32 v136, v56
	v_exp_f32_e32 v137, v57
	v_exp_f32_e32 v138, v58
	v_exp_f32_e32 v139, v59
	v_exp_f32_e32 v140, v60
	v_exp_f32_e32 v141, v61
	v_exp_f32_e32 v142, v62
	v_exp_f32_e32 v143, v63
	v_exp_f32_e32 v144, v64
	v_exp_f32_e32 v145, v65
	v_exp_f32_e32 v114, v34
	v_exp_f32_e32 v115, v35
	v_exp_f32_e32 v116, v36
	v_exp_f32_e32 v117, v37
	v_exp_f32_e32 v118, v38
	v_exp_f32_e32 v119, v39
	v_exp_f32_e32 v120, v40
	v_exp_f32_e32 v121, v41
	v_exp_f32_e32 v122, v42
	v_exp_f32_e32 v123, v43
	v_exp_f32_e32 v124, v44
	v_exp_f32_e32 v125, v45
	v_exp_f32_e32 v126, v46
	v_exp_f32_e32 v127, v47
	v_exp_f32_e32 v128, v48
	v_exp_f32_e32 v129, v49
	s_waitcnt vmcnt(4) lgkmcnt(0)
	s_barrier
	v_mov_b64_e32 v[80:81], v[16:17]
	v_mov_b64_e32 v[48:49], v[16:17]
	v_mov_b64_e32 v[64:65], v[16:17]
	v_mov_b64_e32 v[78:79], v[14:15]
	v_mov_b64_e32 v[76:77], v[12:13]
	v_mov_b64_e32 v[74:75], v[10:11]
	v_mov_b64_e32 v[72:73], v[8:9]
	v_mov_b64_e32 v[70:71], v[6:7]
	v_mov_b64_e32 v[68:69], v[4:5]
	v_mov_b64_e32 v[66:67], v[2:3]
	v_mov_b64_e32 v[46:47], v[14:15]
	v_mov_b64_e32 v[44:45], v[12:13]
	v_mov_b64_e32 v[42:43], v[10:11]
	v_mov_b64_e32 v[40:41], v[8:9]
	v_mov_b64_e32 v[38:39], v[6:7]
	v_mov_b64_e32 v[36:37], v[4:5]
	v_mov_b64_e32 v[34:35], v[2:3]
	v_mov_b64_e32 v[62:63], v[14:15]
	v_mov_b64_e32 v[60:61], v[12:13]
	v_mov_b64_e32 v[58:59], v[10:11]
	v_mov_b64_e32 v[56:57], v[8:9]
	v_mov_b64_e32 v[54:55], v[6:7]
	v_mov_b64_e32 v[52:53], v[4:5]
	v_mov_b64_e32 v[50:51], v[2:3]
	v_mov_b32_e32 v244, 0x23ee8
	ds_read2_b64 v[250:253], v244 offset1:1
	ds_read_b64 v[254:255], v244 offset:16
	s_waitcnt lgkmcnt(0)
	v_readfirstlane_b32 s68, v250
	v_readfirstlane_b32 s69, v251
	v_readfirstlane_b32 s70, v252
	v_readfirstlane_b32 s71, v253
	v_readfirstlane_b32 s72, v254
	v_readfirstlane_b32 s73, v255
	ds_read_b64 v[250:251], v244 offset:40
	s_waitcnt lgkmcnt(0)
	v_readfirstlane_b32 s74, v250
	v_readfirstlane_b32 s75, v251
	s_add_u32 s76, s74, 0x16530000
	s_addc_u32 s77, s75, 0
	s_add_u32 s74, s74, 0xa530000
	s_addc_u32 s75, s75, 0
	v_lshrrev_b32_e32 v25, 3, v214
	v_and_b32_e32 v28, 7, v214
	v_lshlrev_b32_e32 v33, 4, v28
	v_lshl_add_u32 v24, v25, 12, v33
	v_lshl_add_u32 v246, v25, 13, v33
	v_lshlrev_b32_e32 v29, 8, v28
	v_lshl_add_u32 v29, v25, 1, v29
	s_lshl_b32 s2, s40, 11
	s_cmp_lt_u32 s40, 6
	s_mov_b32 s3, 0x21000
	s_cselect_b32 s3, 0x20800, s3
	s_add_i32 s2, s2, s3
	v_add_u32_e32 v29, s2, v29
	v_add_u32_e32 v29, 32, v29
	v_lshl_add_u32 v32, v214, 3, s2
	s_mul_i32 s66, s96, 8
	s_add_i32 s66, s66, s40
	s_cmpk_lt_u32 s36, 0x100
	s_movk_i32 s67, 112
	s_cselect_b32 s67, 112, s67
	s_cselect_b32 s2, 0, 0x7000
	s_add_i32 s66, s66, s2
	s_add_i32 s90, s67, 6
	s_cmp_eq_u32 s67, 0
	s_cselect_b32 s90, -1, s90
	global_load_dword v249, v24, s[68:69]
	global_load_dword v249, v24, s[68:69]

; __device__ __forceinline__ void convert_moe_items(const Ctx& a, int layer, LAS unsigned char* lds, int it0, int it1, int widx, int nw, int wave, int lane) {
;     ...
;     auto decode = [&](int it) { CvtItem d; const int e = it / PER_E; int r = it % PER_E; const size_t eo = ((size_t)layer * NE + e) * (size_t)DM * FE;
;         if (r < I_G)          { d.src = wg + eo; d.dst = WGU; d.N = FE; d.K = DM; d.row_off = e * 2048; d.ilv = 1; }
;         else if (r < 2 * I_G) { r -= I_G; d.src = wu + eo; d.dst = WGU; d.N = FE; d.K = DM; d.row_off = e * 2048 + 128; d.ilv = 1; }
;         else                  { r -= 2 * I_G; d.src = wd + eo; d.dst = WD; d.N = DM; d.K = FE; d.row_off = e * 2048; d.ilv = 0; }
;         const int nblk = d.N / 32; d.k0 = 64 * (r / nblk); d.n0 = 32 * (r % nblk); return d; };
.Lcs_dec_h0:
	s_cmp_lt_u32 s66, 0xa800
	s_cbranch_scc1 .Lcs_id_h0
	s_bitcmp1_b32 s66, 16
	s_cbranch_scc1 .Lcs_id_h0
	s_add_i32 s66, s66, 0xe000

; #define LAS __attribute__((address_space(3)))
;     __device__ __forceinline__ const float* x() const { return (const float*)ld(0); }
;     __device__ __forceinline__ const float* w_gate() const { return (const float*)ld(21); }
;     __device__ __forceinline__ const float* w_up() const { return (const float*)ld(22); }
;     __device__ __forceinline__ const float* w_down() const { return (const float*)ld(23); }
;     __device__ __forceinline__ unsigned char* ws() const { return (unsigned char*)ld(26); }
; __device__ __forceinline__ void convert_moe_items(const Ctx& a, int layer, LAS unsigned char* lds, int it0, int it1, int widx, int nw, int wave, int lane) {
;     LAS float* scr = (LAS float*)(lds + wave * 16384);
;     bf16_t* WGU = (bf16_t*)(a.ws() + WS_WGU + (size_t)layer * WGU_BYTES); bf16_t* WD = (bf16_t*)(a.ws() + WS_WD + (size_t)layer * WD_BYTES);
;     constexpr int I_G = (DM / 64) * (FE / 32), I_D = (FE / 64) * (DM / 32);
;     constexpr int PER_E = 2 * I_G + I_D;
;     const float *wg = a.w_gate(), *wu = a.w_up(), *wd = a.w_down();
;     auto decode = [&](int it) { CvtItem d; const int e = it / PER_E; int r = it % PER_E; const size_t eo = ((size_t)layer * NE + e) * (size_t)DM * FE;
;         if (r < I_G)          { d.src = wg + eo; d.dst = WGU; d.N = FE; d.K = DM; d.row_off = e * 2048; d.ilv = 1; }
;         else if (r < 2 * I_G) { r -= I_G; d.src = wu + eo; d.dst = WGU; d.N = FE; d.K = DM; d.row_off = e * 2048 + 128; d.ilv = 1; }
;         else                  { r -= 2 * I_G; d.src = wd + eo; d.dst = WD; d.N = DM; d.K = FE; d.row_off = e * 2048; d.ilv = 0; }
;         const int nblk = d.N / 32; d.k0 = 64 * (r / nblk); d.n0 = 32 * (r % nblk); return d; };
;     int it = it0 + widx;
;     if (it >= it1) return;
; PHASE_FN ph_topk(int layer, unsigned* dep, const XcdBarrier& bar) { PH_PRO;
;     ...
;     if ((int)blockIdx.x >= NE || G <= NE) { const int widx = (G <= NE) ? gw : ((int)blockIdx.x - NE) * NWAVES + wave, nw = (G <= NE) ? NGW : (G - NE) * NWAVES;
;         if (layer == 0) convert_moe_items(a, 0, lds, L0_A, L0_B, widx, nw, wave, lane); else convert_moe_items(a, 1, lds, L1_A, MOE_ITEMS, widx, nw, wave, lane); } }
.LBB0_1111:
	v_readlane_b32 s0, v248, 6
	s_cmp_gt_i32 s0, 15
	v_readlane_b32 s1, v248, 7
	s_cselect_b64 s[2:3], -1, 0
	s_waitcnt lgkmcnt(0)
	s_cmp_lt_i32 s96, 17
	s_cselect_b64 s[0:1], -1, 0
	s_or_b64 s[2:3], s[2:3], s[0:1]
	s_and_b64 vcc, exec, s[2:3]
	s_cbranch_vccz .LBB0_1158
	v_readlane_b32 s2, v248, 8
	s_lshr_b32 s22, s2, 6
	v_readlane_b32 s2, v248, 6
	s_lshl_b32 s4, s2, 3
	v_readlane_b32 s3, v248, 7
	s_add_i32 s5, s4, 0xffffff80
	s_and_b64 s[2:3], s[0:1], exec
	s_cselect_b32 s2, s4, s5
	s_add_i32 s3, 0, 0x23f10
	v_mov_b32_e32 v1, s3
	s_add_i32 s3, 0, 0x23ee8
	s_waitcnt vmcnt(0)
	v_mov_b32_e32 v2, s3
	s_add_i32 s3, 0, 0x23ef8
	ds_read_b64 v[6:7], v1
	ds_read2_b64 v[2:5], v2 offset1:1
	v_mov_b32_e32 v1, s3
	ds_read_b64 v[8:9], v1
	s_add_i32 s2, s2, s22
	s_waitcnt lgkmcnt(2)
	v_readfirstlane_b32 s3, v7
	v_readfirstlane_b32 s6, v6
	s_waitcnt lgkmcnt(1)
	v_readfirstlane_b32 s26, v3
	v_readfirstlane_b32 s27, v2
	v_readfirstlane_b32 s28, v5
	v_readfirstlane_b32 s29, v4
	s_waitcnt lgkmcnt(0)
	v_readfirstlane_b32 s30, v9
	s_cmpk_gt_i32 s2, 0x7ff
	v_readfirstlane_b32 s31, v8
	s_cbranch_scc1 .LBB0_1158
	s_add_u32 s4, s6, 0x2530000
	s_addc_u32 s5, s3, 0
	s_add_u32 s6, s6, 0x12530000
	s_addc_u32 s7, s3, 0
	s_add_i32 s35, s2, 0x3000
	s_mul_hi_i32 s2, s35, 0x2aaaaaab
	s_lshr_b32 s3, s2, 31
	s_ashr_i32 s2, s2, 9
	s_add_i32 s2, s2, s3
	s_mul_i32 s3, s2, 0xc00
	s_sub_i32 s15, s35, s3
	s_ashr_i32 s3, s2, 31
	s_lshl_b64 s[10:11], s[2:3], 21
	s_lshl_b32 s17, s2, 11
	s_cmpk_gt_i32 s15, 0x3ff
	s_cbranch_scc0 .LBB0_1117
	s_cmpk_gt_u32 s15, 0x7ff
	s_cbranch_scc0 .LBB0_1123
	s_add_i32 s14, s15, 0xfffff800
	s_lshl_b64 s[2:3], s[10:11], 2
	s_add_u32 s2, s31, s2
	s_addc_u32 s3, s30, s3
	s_mov_b32 s25, 1
	s_cbranch_execz .LBB0_1124
	s_movk_i32 s16, 0x800
	s_movk_i32 s33, 0x400
	s_mov_b32 s25, 0
	s_mov_b32 s34, s17
	s_mov_b64 s[8:9], s[6:7]
	s_cbranch_execz .LBB0_1118
	s_branch .LBB0_1119

; __device__ __forceinline__ void cvt_load(const CvtItem& d, f32x4 (&v)[8], int lane) {
;     const float* p = d.src + (size_t)(d.k0 + (lane >> 3)) * d.N + d.n0 + (lane & 7) * 4;
; #pragma unroll
;     for (int q = 0; q < 8; ++q) v[q] = __builtin_nontemporal_load((const f32x4*)(p + (size_t)(8 * q) * d.N));
; }
; __device__ __forceinline__ void convert_moe_items(const Ctx& a, int layer, LAS unsigned char* lds, int it0, int it1, int widx, int nw, int wave, int lane) {
;     ...
;     int it = it0 + widx;
;     if (it >= it1) return;
;     f32x4 va[8], vb[8]; CvtItem da = decode(it), db = da; bool hb = (it + nw < it1);
;     cvt_load(da, va, lane);
;     if (hb) { db = decode(it + nw); cvt_load(db, vb, lane); }
.LBB0_1119:
	s_lshl_b32 s10, s96, 3
	s_add_i32 s11, s10, 0xffffff80
	s_and_b64 s[0:1], s[0:1], exec
	s_cselect_b32 s11, s10, s11
	s_lshr_b32 s12, s16, 5
	v_cvt_f32_i32_e32 v1, s12
	s_sext_i32_i16 s0, s14
	v_cvt_f32_i32_e32 v2, s0
	s_ashr_i32 s0, s0, 30
	v_rcp_iflag_f32_e32 v3, v1
	s_or_b32 s10, s0, 1
	v_lshlrev_b32_e32 v4, 2, v0
	v_and_b32_e32 v4, 28, v4
	v_mul_f32_e32 v3, v2, v3
	v_trunc_f32_e32 v3, v3
	v_fma_f32 v2, -v3, v1, v2
	v_cvt_i32_f32_e32 v3, v3
	v_cmp_ge_f32_e64 s[0:1], |v2|, v1
	s_and_b64 s[0:1], s[0:1], exec
	s_cselect_b32 s0, s10, 0
	v_readfirstlane_b32 s1, v3
	s_add_i32 s0, s1, s0
	s_sext_i32_i16 s1, s0
	s_mul_i32 s0, s0, s12
	s_sub_i32 s0, s14, s0
	s_lshl_b32 s10, s1, 6
	s_sext_i32_i16 s0, s0
	v_lshrrev_b32_e32 v1, 3, v214
	s_lshl_b32 s12, s0, 5
	s_add_i32 s19, s35, s11
	v_or_b32_e32 v2, s10, v1
	s_cmpk_lt_i32 s19, 0x3800
	v_mul_hi_i32_i24_e32 v3, s16, v2
	v_mul_i32_i24_e32 v2, s16, v2
	s_cselect_b64 s[14:15], -1, 0
	s_ashr_i32 s13, s12, 31
	v_lshl_add_u64 v[2:3], v[2:3], 2, s[2:3]
	s_mov_b32 s17, 0
	v_lshl_add_u64 v[2:3], s[12:13], 2, v[2:3]
	v_mov_b32_e32 v67, 0
	v_lshlrev_b32_e32 v66, 2, v4
	s_lshl_b64 s[0:1], s[16:17], 5
	v_lshl_add_u64 v[10:11], v[2:3], 0, v[66:67]
	v_lshl_add_u64 v[12:13], v[10:11], 0, s[0:1]
	v_lshl_add_u64 v[18:19], v[12:13], 0, s[0:1]
	v_lshl_add_u64 v[20:21], v[18:19], 0, s[0:1]
	v_lshl_add_u64 v[26:27], v[20:21], 0, s[0:1]
	v_lshl_add_u64 v[28:29], v[26:27], 0, s[0:1]
	v_lshl_add_u64 v[34:35], v[28:29], 0, s[0:1]
	global_load_dwordx4 v[2:5], v[10:11], off nt
	global_load_dwordx4 v[6:9], v[12:13], off nt
	s_nop 0
	global_load_dwordx4 v[10:13], v[18:19], off nt
	global_load_dwordx4 v[14:17], v[20:21], off nt
	s_nop 0
	global_load_dwordx4 v[18:21], v[26:27], off nt
	global_load_dwordx4 v[22:25], v[28:29], off nt
	v_lshl_add_u64 v[36:37], v[34:35], 0, s[0:1]
	global_load_dwordx4 v[26:29], v[34:35], off nt
	global_load_dwordx4 v[30:33], v[36:37], off nt
	s_cmpk_gt_i32 s19, 0x37ff
	s_mov_b64 s[0:1], s[8:9]
	s_mov_b32 s37, s33
	s_mov_b32 s38, s34
	s_mov_b32 s36, s25
	s_mov_b32 s18, s10
	s_mov_b32 s20, s12
	s_cbranch_scc1 .LBB0_1134
	s_mul_hi_i32 s0, s19, 0x2aaaaaab
	s_lshr_b32 s1, s0, 31
	s_ashr_i32 s0, s0, 9
	s_add_i32 s0, s0, s1
	s_mul_i32 s1, s0, 0xc00
	s_sub_i32 s17, s19, s1
	s_ashr_i32 s1, s0, 31
	s_lshl_b64 s[18:19], s[0:1], 21
	s_lshl_b32 s23, s0, 11
	s_cmpk_gt_i32 s17, 0x3ff
	s_cbranch_scc0 .LBB0_1125
	s_cmpk_gt_u32 s17, 0x7ff
	s_cbranch_scc0 .LBB0_1126
	s_add_i32 s13, s17, 0xfffff800
	s_lshl_b64 s[0:1], s[18:19], 2
	s_add_u32 s2, s31, s0
	s_addc_u32 s3, s30, s1
	s_mov_b64 s[0:1], 0
	s_branch .LBB0_1127

; #define LAS __attribute__((address_space(3)))
; __device__ __forceinline__ unsigned pk2(float lo, float hi) { return f2bf(lo) | (f2bf(hi) << 16); }
;     __device__ __forceinline__ const float* x() const { return (const float*)ld(0); }
;     __device__ __forceinline__ const float* c() const { return (const float*)ld(1); }
; template <bool NT = true> __device__ __forceinline__ void cvt_store(const CvtItem& d, const f32x4 (&v)[8], LAS float* scr, int lane) {
;     const int rr = lane >> 3, c4 = (lane & 7) * 4;
; #pragma unroll
;     for (int q = 0; q < 8; ++q) { LAS float* t = scr + (8 * q + rr) * 33 + c4; t[0] = v[q].x; t[1] = v[q].y; t[2] = v[q].z; t[3] = v[q].w; }
;     asm volatile("s_waitcnt lgkmcnt(0)" ::: "memory");
;     const int c = lane & 7;
; #pragma unroll
;     for (int j = 0; j < 4; ++j) { const int n = (lane >> 3) + 8 * j; const LAS float* s = scr + (8 * c) * 33 + n;
;         u32x4 o; o.x = pk2(s[0 * 33], s[1 * 33]); o.y = pk2(s[2 * 33], s[3 * 33]); o.z = pk2(s[4 * 33], s[5 * 33]); o.w = pk2(s[6 * 33], s[7 * 33]);
;         const int ng = d.n0 + n, drow = d.row_off + (d.ilv ? ((ng >> 7) * 256 + (ng & 127)) : ng);
;         if (NT) __builtin_nontemporal_store(o, (u32x4*)(d.dst + (size_t)drow * d.K + d.k0 + 8 * c)); else *(u32x4*)(d.dst + (size_t)drow * d.K + d.k0 + 8 * c) = o; }
;     asm volatile("s_waitcnt lgkmcnt(0)" ::: "memory");
; __device__ __forceinline__ void convert_moe_items(const Ctx& a, int layer, LAS unsigned char* lds, int it0, int it1, int widx, int nw, int wave, int lane) {
;     ...
;         it += 2 * nw; const bool ha = (it < it1);
;         if (ha) { da = decode(it); cvt_load(da, va, lane); }
.Lcvt_p6_t:
	v_add_u32_e32 v79, 0x420, v74
	v_add_u32_e32 v80, 0x428, v74
	v_add_u32_e32 v81, 0x840, v74
	v_add_u32_e32 v82, 0x848, v74
	v_add_u32_e32 v83, 0xc60, v74
	v_add_u32_e32 v84, 0xc68, v74
	v_add_u32_e32 v85, 0x1080, v74
	v_add_u32_e32 v86, 0x1088, v74
	v_add_u32_e32 v87, 0x14a0, v74
	v_add_u32_e32 v88, 0x14a8, v74
	v_add_u32_e32 v89, 0x18c0, v74
	v_add_u32_e32 v90, 0x18c8, v74
	v_add_u32_e32 v91, 0x1ce0, v74
	v_add_u32_e32 v92, 0x1ce8, v74
	s_waitcnt vmcnt(15)
	ds_write2_b32 v74, v2, v3 offset1:1
	ds_write2_b32 v74, v4, v5 offset0:2 offset1:3
	s_waitcnt vmcnt(14)
	ds_write2_b32 v79, v6, v7 offset1:1
	ds_write2_b32 v80, v8, v9 offset1:1
	s_waitcnt vmcnt(13)
	ds_write2_b32 v81, v10, v11 offset1:1
	ds_write2_b32 v82, v12, v13 offset1:1
	s_waitcnt vmcnt(12)
	ds_write2_b32 v83, v14, v15 offset1:1
	ds_write2_b32 v84, v16, v17 offset1:1
	s_waitcnt vmcnt(11)
	ds_write2_b32 v85, v18, v19 offset1:1
	ds_write2_b32 v86, v20, v21 offset1:1
	s_waitcnt vmcnt(10)
	ds_write2_b32 v87, v22, v23 offset1:1
	ds_write2_b32 v88, v24, v25 offset1:1
	s_waitcnt vmcnt(9)
	ds_write2_b32 v89, v26, v27 offset1:1
	ds_write2_b32 v90, v28, v29 offset1:1
	s_waitcnt vmcnt(8)
	ds_write2_b32 v91, v30, v31 offset1:1
	ds_write2_b32 v92, v32, v33 offset1:1
	s_waitcnt lgkmcnt(0)
	ds_read2_b32 v[98:99], v73 offset1:8
	ds_read2_b32 v[100:101], v73 offset0:33 offset1:41
	ds_read2_b32 v[102:103], v73 offset0:66 offset1:74
	ds_read2_b32 v[104:105], v73 offset0:99 offset1:107
	ds_read2_b32 v[106:107], v73 offset0:132 offset1:140
	s_waitcnt lgkmcnt(4)
	v_bfe_u32 v67, v98, 16, 1
	v_add3_u32 v67, v98, v67, s41
	s_waitcnt lgkmcnt(3)
	v_bfe_u32 v93, v100, 16, 1
	v_lshrrev_b32_e32 v67, 16, v67
	v_add3_u32 v93, v100, v93, s41
	ds_read2_b32 v[108:109], v73 offset0:165 offset1:173
	v_and_or_b32 v94, v93, s42, v67
	s_waitcnt lgkmcnt(3)
	v_bfe_u32 v67, v102, 16, 1
	v_add3_u32 v67, v102, v67, s41
	s_waitcnt lgkmcnt(2)
	v_bfe_u32 v93, v104, 16, 1
	ds_read2_b32 v[110:111], v73 offset0:198 offset1:206
	v_lshrrev_b32_e32 v67, 16, v67
	v_add3_u32 v93, v104, v93, s41
	ds_read2_b32 v[112:113], v73 offset0:231 offset1:239
	v_and_or_b32 v95, v93, s42, v67
	s_waitcnt lgkmcnt(3)
	v_bfe_u32 v67, v106, 16, 1
	v_add3_u32 v67, v106, v67, s41
	s_waitcnt lgkmcnt(2)
	v_bfe_u32 v93, v108, 16, 1
	v_lshrrev_b32_e32 v67, 16, v67
	v_add3_u32 v93, v108, v93, s41
	v_and_or_b32 v96, v93, s42, v67
	s_waitcnt lgkmcnt(1)
	v_bfe_u32 v67, v110, 16, 1
	v_add3_u32 v67, v110, v67, s41
	s_waitcnt lgkmcnt(0)
	v_bfe_u32 v93, v112, 16, 1
	s_cmp_eq_u32 s25, 0
	v_lshrrev_b32_e32 v67, 16, v67
	v_add3_u32 v93, v112, v93, s41
	s_cselect_b64 vcc, -1, 0
	s_lshl_b32 s2, s12, 1
	v_and_or_b32 v97, v93, s42, v67
	s_and_b32 s13, s2, 0xffffff00
	v_bitop3_b32 v93, s12, v75, v1 bitop3:0xc8
	v_or_b32_e32 v67, s12, v1
	v_or_b32_e32 v93, s13, v93
	v_cndmask_b32_e32 v67, v93, v67, vcc
	v_add_u32_e32 v67, s34, v67
	v_mad_u64_u32 v[114:115], s[2:3], v67, s33, 0
	v_ashrrev_i32_e32 v93, 31, v67
	v_mov_b32_e32 v98, v115
	v_mad_u64_u32 v[116:117], s[2:3], v93, s33, v[98:99]
	v_mov_b32_e32 v115, v116
	s_ashr_i32 s11, s10, 31
	v_lshl_add_u64 v[114:115], v[114:115], 1, s[8:9]
	s_lshl_b64 s[2:3], s[10:11], 1
	v_bfe_u32 v67, v99, 16, 1
	v_lshl_add_u64 v[114:115], v[114:115], 0, s[2:3]
	v_add3_u32 v67, v99, v67, s41
	v_bfe_u32 v93, v101, 16, 1
	v_lshl_add_u64 v[114:115], v[114:115], 0, v[68:69]
	v_lshrrev_b32_e32 v67, 16, v67
	v_add3_u32 v93, v101, v93, s41
	global_store_dwordx4 v[114:115], v[94:97], off nt
	s_add_i32 s44, s35, s39
	s_cmpk_gt_i32 s44, 0x37ff
	v_and_or_b32 v94, v93, s42, v67
	v_bfe_u32 v67, v103, 16, 1
	v_add3_u32 v67, v103, v67, s41
	v_bfe_u32 v93, v105, 16, 1
	v_lshrrev_b32_e32 v67, 16, v67
	v_add3_u32 v93, v105, v93, s41
	v_and_or_b32 v95, v93, s42, v67
	v_bfe_u32 v67, v107, 16, 1
	v_add3_u32 v67, v107, v67, s41
	v_bfe_u32 v93, v109, 16, 1
	v_lshrrev_b32_e32 v67, 16, v67
	v_add3_u32 v93, v109, v93, s41
	v_and_or_b32 v96, v93, s42, v67
	v_bfe_u32 v67, v111, 16, 1
	v_add3_u32 v67, v111, v67, s41
	v_bfe_u32 v93, v113, 16, 1
	v_lshrrev_b32_e32 v67, 16, v67
	v_add3_u32 v93, v113, v93, s41
	v_and_or_b32 v97, v93, s42, v67
	v_bitop3_b32 v93, s12, v76, v70 bitop3:0xc8
	v_or_b32_e32 v67, s12, v70
	v_or_b32_e32 v93, s13, v93
	v_cndmask_b32_e32 v67, v93, v67, vcc
	v_add_u32_e32 v67, s34, v67
	v_mad_u64_u32 v[98:99], s[22:23], v67, s33, 0
	v_ashrrev_i32_e32 v93, 31, v67
	v_mov_b32_e32 v100, v99
	v_mad_u64_u32 v[100:101], s[22:23], v93, s33, v[100:101]
	v_mov_b32_e32 v99, v100
	v_lshl_add_u64 v[98:99], v[98:99], 1, s[8:9]
	v_lshl_add_u64 v[98:99], v[98:99], 0, s[2:3]
	ds_read2_b32 v[100:101], v73 offset0:16 offset1:24
	v_lshl_add_u64 v[98:99], v[98:99], 0, v[68:69]
	global_store_dwordx4 v[98:99], v[94:97], off nt
	ds_read2_b32 v[98:99], v73 offset0:49 offset1:57
	ds_read2_b32 v[102:103], v73 offset0:82 offset1:90
	ds_read2_b32 v[104:105], v73 offset0:115 offset1:123
	s_waitcnt lgkmcnt(3)
; #define LAS __attribute__((address_space(3)))
; __device__ __forceinline__ unsigned pk2(float lo, float hi) { return f2bf(lo) | (f2bf(hi) << 16); }
;     __device__ __forceinline__ const float* x() const { return (const float*)ld(0); }
;     __device__ __forceinline__ const float* c() const { return (const float*)ld(1); }
; template <bool NT = true> __device__ __forceinline__ void cvt_store(const CvtItem& d, const f32x4 (&v)[8], LAS float* scr, int lane) {
;     ...
;     for (int j = 0; j < 4; ++j) { const int n = (lane >> 3) + 8 * j; const LAS float* s = scr + (8 * c) * 33 + n;
;         u32x4 o; o.x = pk2(s[0 * 33], s[1 * 33]); o.y = pk2(s[2 * 33], s[3 * 33]); o.z = pk2(s[4 * 33], s[5 * 33]); o.w = pk2(s[6 * 33], s[7 * 33]);
;         const int ng = d.n0 + n, drow = d.row_off + (d.ilv ? ((ng >> 7) * 256 + (ng & 127)) : ng);
;         if (NT) __builtin_nontemporal_store(o, (u32x4*)(d.dst + (size_t)drow * d.K + d.k0 + 8 * c)); else *(u32x4*)(d.dst + (size_t)drow * d.K + d.k0 + 8 * c) = o; }
;     asm volatile("s_waitcnt lgkmcnt(0)" ::: "memory");
; __device__ __forceinline__ void convert_moe_items(const Ctx& a, int layer, LAS unsigned char* lds, int it0, int it1, int widx, int nw, int wave, int lane) {
;     ...
;         it += 2 * nw; const bool ha = (it < it1);
;         if (ha) { da = decode(it); cvt_load(da, va, lane); }
;         if (!hb) break;
;         cvt_store(db, vb, scr, lane);
;         hb = (it + nw < it1);
;         if (hb) { db = decode(it + nw); cvt_load(db, vb, lane); }
	v_bfe_u32 v67, v100, 16, 1
	v_add3_u32 v67, v100, v67, s41
	s_waitcnt lgkmcnt(2)
	v_bfe_u32 v93, v98, 16, 1
	ds_read2_b32 v[106:107], v73 offset0:148 offset1:156
	v_lshrrev_b32_e32 v67, 16, v67
	v_add3_u32 v93, v98, v93, s41
	ds_read2_b32 v[108:109], v73 offset0:181 offset1:189
	v_and_or_b32 v94, v93, s42, v67
	s_waitcnt lgkmcnt(3)
	v_bfe_u32 v67, v102, 16, 1
	v_add3_u32 v67, v102, v67, s41
	s_waitcnt lgkmcnt(2)
	v_bfe_u32 v93, v104, 16, 1
	ds_read2_b32 v[110:111], v73 offset0:214 offset1:222
	v_lshrrev_b32_e32 v67, 16, v67
	v_add3_u32 v93, v104, v93, s41
	ds_read2_b32 v[112:113], v73 offset0:247 offset1:255
	v_and_or_b32 v95, v93, s42, v67
	s_waitcnt lgkmcnt(3)
	v_bfe_u32 v67, v106, 16, 1
	v_add3_u32 v67, v106, v67, s41
	s_waitcnt lgkmcnt(2)
	v_bfe_u32 v93, v108, 16, 1
	v_lshrrev_b32_e32 v67, 16, v67
	v_add3_u32 v93, v108, v93, s41
	v_and_or_b32 v96, v93, s42, v67
	s_waitcnt lgkmcnt(1)
	v_bfe_u32 v67, v110, 16, 1
	v_add3_u32 v67, v110, v67, s41
	s_waitcnt lgkmcnt(0)
	v_bfe_u32 v93, v112, 16, 1
	v_lshrrev_b32_e32 v67, 16, v67
	v_add3_u32 v93, v112, v93, s41
	v_and_or_b32 v97, v93, s42, v67
	v_bitop3_b32 v93, s12, v77, v71 bitop3:0xc8
	v_or_b32_e32 v67, s12, v71
	v_or_b32_e32 v93, s13, v93
	v_cndmask_b32_e32 v67, v93, v67, vcc
	v_add_u32_e32 v67, s34, v67
	v_mad_u64_u32 v[114:115], s[22:23], v67, s33, 0
	v_ashrrev_i32_e32 v93, 31, v67
	v_mov_b32_e32 v98, v115
	v_mad_u64_u32 v[116:117], s[22:23], v93, s33, v[98:99]
	v_mov_b32_e32 v115, v116
	v_lshl_add_u64 v[114:115], v[114:115], 1, s[8:9]
	v_bfe_u32 v67, v101, 16, 1
	v_lshl_add_u64 v[114:115], v[114:115], 0, s[2:3]
	v_add3_u32 v67, v101, v67, s41
	v_bfe_u32 v93, v99, 16, 1
	v_lshl_add_u64 v[114:115], v[114:115], 0, v[68:69]
	v_lshrrev_b32_e32 v67, 16, v67
	v_add3_u32 v93, v99, v93, s41
	global_store_dwordx4 v[114:115], v[94:97], off nt
	s_nop 1
	v_and_or_b32 v94, v93, s42, v67
	v_bfe_u32 v67, v103, 16, 1
	v_add3_u32 v67, v103, v67, s41
	v_bfe_u32 v93, v105, 16, 1
	v_lshrrev_b32_e32 v67, 16, v67
	v_add3_u32 v93, v105, v93, s41
	v_and_or_b32 v95, v93, s42, v67
	v_bfe_u32 v67, v107, 16, 1
	v_add3_u32 v67, v107, v67, s41
	v_bfe_u32 v93, v109, 16, 1
	v_lshrrev_b32_e32 v67, 16, v67
	v_add3_u32 v93, v109, v93, s41
	v_and_or_b32 v96, v93, s42, v67
	v_bfe_u32 v67, v111, 16, 1
	v_add3_u32 v67, v111, v67, s41
	v_bfe_u32 v93, v113, 16, 1
	v_lshrrev_b32_e32 v67, 16, v67
	v_add3_u32 v93, v113, v93, s41
	v_and_or_b32 v97, v93, s42, v67
	v_bitop3_b32 v93, s12, v78, v72 bitop3:0xc8
	v_or_b32_e32 v67, s12, v72
	v_or_b32_e32 v93, s13, v93
	v_cndmask_b32_e32 v67, v93, v67, vcc
	v_add_u32_e32 v67, s34, v67
	v_mad_u64_u32 v[98:99], s[22:23], v67, s33, 0
	v_ashrrev_i32_e32 v93, 31, v67
	v_mov_b32_e32 v100, v99
	v_mad_u64_u32 v[100:101], s[22:23], v93, s33, v[100:101]
	v_mov_b32_e32 v99, v100
	v_lshl_add_u64 v[98:99], v[98:99], 1, s[8:9]
	v_lshl_add_u64 v[98:99], v[98:99], 0, s[2:3]
	v_lshl_add_u64 v[98:99], v[98:99], 0, v[68:69]
	global_store_dwordx4 v[98:99], v[94:97], off nt
	s_waitcnt lgkmcnt(0)
	s_cselect_b64 s[22:23], -1, 0
	s_and_b64 vcc, exec, s[22:23]
	s_cbranch_vccnz .LBB0_1147
	s_mul_hi_i32 s2, s44, 0x2aaaaaab
	s_lshr_b32 s3, s2, 31
	s_ashr_i32 s2, s2, 9
	s_add_i32 s24, s2, s3
	s_mul_i32 s2, s24, 0xfffff400
	s_ashr_i32 s25, s24, 31
	s_add_i32 s21, s44, s2
	s_lshl_b64 s[10:11], s[24:25], 21
	s_lshl_b32 s45, s24, 11
	s_cmpk_gt_i32 s21, 0x3ff
	s_mov_b64 s[12:13], -1
	s_cbranch_scc0 .LBB0_1144
	s_mul_i32 s2, s24, 0xc00
	s_sub_i32 s12, s44, s2
	s_cmpk_gt_u32 s21, 0x7ff
	s_mov_b64 s[8:9], -1
	s_cbranch_scc0 .LBB0_1142
	s_add_i32 s19, s12, 0xfffff800
	s_lshl_b64 s[2:3], s[10:11], 2
	s_add_u32 s2, s31, s2
	s_addc_u32 s3, s30, s3
	s_mov_b64 s[8:9], 0

; #define LAS __attribute__((address_space(3)))
; __device__ __forceinline__ unsigned pk2(float lo, float hi) { return f2bf(lo) | (f2bf(hi) << 16); }
;     __device__ __forceinline__ const float* x() const { return (const float*)ld(0); }
;     __device__ __forceinline__ const float* c() const { return (const float*)ld(1); }
; template <bool NT = true> __device__ __forceinline__ void cvt_store(const CvtItem& d, const f32x4 (&v)[8], LAS float* scr, int lane) {
;     const int rr = lane >> 3, c4 = (lane & 7) * 4;
; #pragma unroll
;     for (int q = 0; q < 8; ++q) { LAS float* t = scr + (8 * q + rr) * 33 + c4; t[0] = v[q].x; t[1] = v[q].y; t[2] = v[q].z; t[3] = v[q].w; }
;     asm volatile("s_waitcnt lgkmcnt(0)" ::: "memory");
;     const int c = lane & 7;
; #pragma unroll
;     for (int j = 0; j < 4; ++j) { const int n = (lane >> 3) + 8 * j; const LAS float* s = scr + (8 * c) * 33 + n;
;         u32x4 o; o.x = pk2(s[0 * 33], s[1 * 33]); o.y = pk2(s[2 * 33], s[3 * 33]); o.z = pk2(s[4 * 33], s[5 * 33]); o.w = pk2(s[6 * 33], s[7 * 33]);
;         const int ng = d.n0 + n, drow = d.row_off + (d.ilv ? ((ng >> 7) * 256 + (ng & 127)) : ng);
;         if (NT) __builtin_nontemporal_store(o, (u32x4*)(d.dst + (size_t)drow * d.K + d.k0 + 8 * c)); else *(u32x4*)(d.dst + (size_t)drow * d.K + d.k0 + 8 * c) = o; }
;     asm volatile("s_waitcnt lgkmcnt(0)" ::: "memory");
.Lcvt_p6_m:
	s_waitcnt vmcnt(12)
	ds_write2_b32 v74, v34, v35 offset1:1
	ds_write2_b32 v74, v36, v37 offset0:2 offset1:3
	ds_write2_b32 v79, v38, v39 offset1:1
	ds_write2_b32 v80, v40, v41 offset1:1
	ds_write2_b32 v81, v42, v43 offset1:1
	ds_write2_b32 v82, v44, v45 offset1:1
	ds_write2_b32 v83, v46, v47 offset1:1
	ds_write2_b32 v84, v48, v49 offset1:1
	ds_write2_b32 v85, v50, v51 offset1:1
	ds_write2_b32 v86, v52, v53 offset1:1
	ds_write2_b32 v87, v54, v55 offset1:1
	ds_write2_b32 v88, v56, v57 offset1:1
	ds_write2_b32 v89, v58, v59 offset1:1
	ds_write2_b32 v90, v60, v61 offset1:1
	ds_write2_b32 v91, v62, v63 offset1:1
	ds_write2_b32 v92, v64, v65 offset1:1
	s_waitcnt lgkmcnt(0)
	ds_read2_b32 v[84:85], v73 offset1:8
	ds_read2_b32 v[86:87], v73 offset0:33 offset1:41
	ds_read2_b32 v[88:89], v73 offset0:66 offset1:74
	ds_read2_b32 v[90:91], v73 offset0:99 offset1:107
	ds_read2_b32 v[92:93], v73 offset0:132 offset1:140
	s_waitcnt lgkmcnt(4)
	v_bfe_u32 v67, v84, 16, 1
	v_add3_u32 v67, v84, v67, s41
	s_waitcnt lgkmcnt(3)
	v_bfe_u32 v79, v86, 16, 1
	v_lshrrev_b32_e32 v67, 16, v67
	v_add3_u32 v79, v86, v79, s41
	ds_read2_b32 v[94:95], v73 offset0:165 offset1:173
	v_and_or_b32 v80, v79, s42, v67
	s_waitcnt lgkmcnt(3)
	v_bfe_u32 v67, v88, 16, 1
	v_add3_u32 v67, v88, v67, s41
	s_waitcnt lgkmcnt(2)
	v_bfe_u32 v79, v90, 16, 1
	ds_read2_b32 v[96:97], v73 offset0:198 offset1:206
	v_lshrrev_b32_e32 v67, 16, v67
	v_add3_u32 v79, v90, v79, s41
	ds_read2_b32 v[98:99], v73 offset0:231 offset1:239
	v_and_or_b32 v81, v79, s42, v67
	s_waitcnt lgkmcnt(3)
	v_bfe_u32 v67, v92, 16, 1
	v_add3_u32 v67, v92, v67, s41
	s_waitcnt lgkmcnt(2)
	v_bfe_u32 v79, v94, 16, 1
	v_lshrrev_b32_e32 v67, 16, v67
	v_add3_u32 v79, v94, v79, s41
	v_and_or_b32 v82, v79, s42, v67
	s_waitcnt lgkmcnt(1)
	v_bfe_u32 v67, v96, 16, 1
	v_add3_u32 v67, v96, v67, s41
	s_waitcnt lgkmcnt(0)
	v_bfe_u32 v79, v98, 16, 1
	v_lshrrev_b32_e32 v67, 16, v67
	v_add3_u32 v79, v98, v79, s41
	v_and_or_b32 v83, v79, s42, v67
	v_add_u32_e32 v67, s20, v1
	s_cmp_eq_u32 s36, 0
	v_lshlrev_b32_e32 v79, 1, v67
	v_and_b32_e32 v84, 0x7f, v67
	v_and_or_b32 v79, v79, s43, v84
	s_cselect_b64 vcc, -1, 0
	v_cndmask_b32_e32 v67, v79, v67, vcc
	v_add_u32_e32 v67, s38, v67
	v_mad_u64_u32 v[100:101], s[2:3], v67, s37, 0
	v_ashrrev_i32_e32 v79, 31, v67
	v_mov_b32_e32 v84, v101
	v_mad_u64_u32 v[102:103], s[2:3], v79, s37, v[84:85]
	v_mov_b32_e32 v101, v102
	s_ashr_i32 s19, s18, 31
	v_lshl_add_u64 v[100:101], v[100:101], 1, s[0:1]
	s_lshl_b64 s[2:3], s[18:19], 1
	v_bfe_u32 v67, v85, 16, 1
	v_lshl_add_u64 v[100:101], v[100:101], 0, s[2:3]
	v_add3_u32 v67, v85, v67, s41
	v_bfe_u32 v79, v87, 16, 1
	v_lshl_add_u64 v[100:101], v[100:101], 0, v[68:69]
	v_lshrrev_b32_e32 v67, 16, v67
	v_add3_u32 v79, v87, v79, s41
	global_store_dwordx4 v[100:101], v[80:83], off nt
	s_nop 1
	v_and_or_b32 v80, v79, s42, v67
	v_bfe_u32 v67, v89, 16, 1
	v_add3_u32 v67, v89, v67, s41
	v_bfe_u32 v79, v91, 16, 1
	v_lshrrev_b32_e32 v67, 16, v67
	v_add3_u32 v79, v91, v79, s41
	v_and_or_b32 v81, v79, s42, v67
	v_bfe_u32 v67, v93, 16, 1
	v_add3_u32 v67, v93, v67, s41
	v_bfe_u32 v79, v95, 16, 1
	v_lshrrev_b32_e32 v67, 16, v67
	v_add3_u32 v79, v95, v79, s41
	v_and_or_b32 v82, v79, s42, v67
	v_bfe_u32 v67, v97, 16, 1
	v_add3_u32 v67, v97, v67, s41
	v_bfe_u32 v79, v99, 16, 1
	v_lshrrev_b32_e32 v67, 16, v67
	v_add3_u32 v79, v99, v79, s41
	v_and_or_b32 v83, v79, s42, v67
	v_add_u32_e32 v67, s20, v70
	v_lshlrev_b32_e32 v79, 1, v67
	v_and_b32_e32 v84, 0x7f, v67
	v_and_or_b32 v79, v79, s43, v84
	v_cndmask_b32_e32 v67, v79, v67, vcc
	v_add_u32_e32 v67, s38, v67
	v_mad_u64_u32 v[84:85], s[14:15], v67, s37, 0
	v_ashrrev_i32_e32 v79, 31, v67
	v_mov_b32_e32 v86, v85
	v_mad_u64_u32 v[86:87], s[14:15], v79, s37, v[86:87]
	v_mov_b32_e32 v85, v86
	v_lshl_add_u64 v[84:85], v[84:85], 1, s[0:1]
	v_lshl_add_u64 v[84:85], v[84:85], 0, s[2:3]
	ds_read2_b32 v[86:87], v73 offset0:16 offset1:24
	v_lshl_add_u64 v[84:85], v[84:85], 0, v[68:69]
	global_store_dwordx4 v[84:85], v[80:83], off nt
	ds_read2_b32 v[84:85], v73 offset0:49 offset1:57
	ds_read2_b32 v[88:89], v73 offset0:82 offset1:90
	ds_read2_b32 v[90:91], v73 offset0:115 offset1:123
	s_waitcnt lgkmcnt(3)
; #define LAS __attribute__((address_space(3)))
; __device__ __forceinline__ unsigned pk2(float lo, float hi) { return f2bf(lo) | (f2bf(hi) << 16); }
;     __device__ __forceinline__ const float* x() const { return (const float*)ld(0); }
;     __device__ __forceinline__ const float* c() const { return (const float*)ld(1); }
; template <bool NT = true> __device__ __forceinline__ void cvt_store(const CvtItem& d, const f32x4 (&v)[8], LAS float* scr, int lane) {
;     ...
;     for (int j = 0; j < 4; ++j) { const int n = (lane >> 3) + 8 * j; const LAS float* s = scr + (8 * c) * 33 + n;
;         u32x4 o; o.x = pk2(s[0 * 33], s[1 * 33]); o.y = pk2(s[2 * 33], s[3 * 33]); o.z = pk2(s[4 * 33], s[5 * 33]); o.w = pk2(s[6 * 33], s[7 * 33]);
;         const int ng = d.n0 + n, drow = d.row_off + (d.ilv ? ((ng >> 7) * 256 + (ng & 127)) : ng);
;         if (NT) __builtin_nontemporal_store(o, (u32x4*)(d.dst + (size_t)drow * d.K + d.k0 + 8 * c)); else *(u32x4*)(d.dst + (size_t)drow * d.K + d.k0 + 8 * c) = o; }
;     asm volatile("s_waitcnt lgkmcnt(0)" ::: "memory");
; __device__ __forceinline__ void convert_moe_items(const Ctx& a, int layer, LAS unsigned char* lds, int it0, int it1, int widx, int nw, int wave, int lane) {
;     ...
;         cvt_store(db, vb, scr, lane);
;         hb = (it + nw < it1);
;         if (hb) { db = decode(it + nw); cvt_load(db, vb, lane); }
;         if (!ha) break;
	v_bfe_u32 v67, v86, 16, 1
	v_add3_u32 v67, v86, v67, s41
	s_waitcnt lgkmcnt(2)
	v_bfe_u32 v79, v84, 16, 1
	ds_read2_b32 v[92:93], v73 offset0:148 offset1:156
	v_lshrrev_b32_e32 v67, 16, v67
	v_add3_u32 v79, v84, v79, s41
	ds_read2_b32 v[94:95], v73 offset0:181 offset1:189
	v_and_or_b32 v80, v79, s42, v67
	s_waitcnt lgkmcnt(3)
	v_bfe_u32 v67, v88, 16, 1
	v_add3_u32 v67, v88, v67, s41
	s_waitcnt lgkmcnt(2)
	v_bfe_u32 v79, v90, 16, 1
	ds_read2_b32 v[96:97], v73 offset0:214 offset1:222
	v_lshrrev_b32_e32 v67, 16, v67
	v_add3_u32 v79, v90, v79, s41
	ds_read2_b32 v[98:99], v73 offset0:247 offset1:255
	v_and_or_b32 v81, v79, s42, v67
	s_waitcnt lgkmcnt(3)
	v_bfe_u32 v67, v92, 16, 1
	v_add3_u32 v67, v92, v67, s41
	s_waitcnt lgkmcnt(2)
	v_bfe_u32 v79, v94, 16, 1
	v_lshrrev_b32_e32 v67, 16, v67
	v_add3_u32 v79, v94, v79, s41
	v_and_or_b32 v82, v79, s42, v67
	s_waitcnt lgkmcnt(1)
	v_bfe_u32 v67, v96, 16, 1
	v_add3_u32 v67, v96, v67, s41
	s_waitcnt lgkmcnt(0)
	v_bfe_u32 v79, v98, 16, 1
	v_lshrrev_b32_e32 v67, 16, v67
	v_add3_u32 v79, v98, v79, s41
	v_and_or_b32 v83, v79, s42, v67
	v_add_u32_e32 v67, s20, v71
	v_lshlrev_b32_e32 v79, 1, v67
	v_and_b32_e32 v84, 0x7f, v67
	v_and_or_b32 v79, v79, s43, v84
	v_cndmask_b32_e32 v67, v79, v67, vcc
	v_add_u32_e32 v67, s38, v67
	v_mad_u64_u32 v[100:101], s[14:15], v67, s37, 0
	v_ashrrev_i32_e32 v79, 31, v67
	v_mov_b32_e32 v84, v101
	v_mad_u64_u32 v[102:103], s[14:15], v79, s37, v[84:85]
	v_mov_b32_e32 v101, v102
	v_lshl_add_u64 v[100:101], v[100:101], 1, s[0:1]
	v_bfe_u32 v67, v87, 16, 1
	v_lshl_add_u64 v[100:101], v[100:101], 0, s[2:3]
	v_add3_u32 v67, v87, v67, s41
	v_bfe_u32 v79, v85, 16, 1
	v_lshl_add_u64 v[100:101], v[100:101], 0, v[68:69]
	v_lshrrev_b32_e32 v67, 16, v67
	v_add3_u32 v79, v85, v79, s41
	global_store_dwordx4 v[100:101], v[80:83], off nt
	s_nop 1
	v_and_or_b32 v80, v79, s42, v67
	v_bfe_u32 v67, v89, 16, 1
	v_add3_u32 v67, v89, v67, s41
	v_bfe_u32 v79, v91, 16, 1
	v_lshrrev_b32_e32 v67, 16, v67
	v_add3_u32 v79, v91, v79, s41
	v_and_or_b32 v81, v79, s42, v67
	v_bfe_u32 v67, v93, 16, 1
	v_add3_u32 v67, v93, v67, s41
	v_bfe_u32 v79, v95, 16, 1
	v_lshrrev_b32_e32 v67, 16, v67
	v_add3_u32 v79, v95, v79, s41
	v_and_or_b32 v82, v79, s42, v67
	v_bfe_u32 v67, v97, 16, 1
	v_add3_u32 v67, v97, v67, s41
	v_bfe_u32 v79, v99, 16, 1
	v_lshrrev_b32_e32 v67, 16, v67
	v_add3_u32 v79, v99, v79, s41
	v_and_or_b32 v83, v79, s42, v67
	v_add_u32_e32 v67, s20, v72
	v_lshlrev_b32_e32 v79, 1, v67
	v_and_b32_e32 v84, 0x7f, v67
	v_and_or_b32 v79, v79, s43, v84
	v_cndmask_b32_e32 v67, v79, v67, vcc
	v_add_u32_e32 v67, s38, v67
	v_mad_u64_u32 v[84:85], s[14:15], v67, s37, 0
	v_ashrrev_i32_e32 v79, 31, v67
	v_mov_b32_e32 v86, v85
	v_mad_u64_u32 v[86:87], s[14:15], v79, s37, v[86:87]
	v_mov_b32_e32 v85, v86
	v_lshl_add_u64 v[84:85], v[84:85], 1, s[0:1]
	v_lshl_add_u64 v[84:85], v[84:85], 0, s[2:3]
	v_lshl_add_u64 v[84:85], v[84:85], 0, v[68:69]
	global_store_dwordx4 v[84:85], v[80:83], off nt
	s_add_i32 s2, s40, s35
	s_waitcnt lgkmcnt(0)
	s_cmpk_lt_i32 s2, 0x3800
	s_cselect_b64 s[14:15], -1, 0
	s_cmpk_gt_i32 s2, 0x37ff
	s_cbranch_scc1 .LBB0_1136
	s_mul_hi_i32 s0, s2, 0x2aaaaaab
	s_lshr_b32 s1, s0, 31
	s_ashr_i32 s0, s0, 9
	s_add_i32 s0, s0, s1
	s_mul_i32 s1, s0, 0xc00
	s_sub_i32 s13, s2, s1
	s_ashr_i32 s1, s0, 31
	s_lshl_b64 s[18:19], s[0:1], 21
	s_lshl_b32 s24, s0, 11
	s_cmpk_gt_i32 s13, 0x3ff
	s_mov_b64 s[20:21], -1
	s_cbranch_scc0 .LBB0_1154
	s_cmpk_gt_u32 s13, 0x7ff
	s_mov_b64 s[0:1], -1
	s_cbranch_scc0 .LBB0_1152
	s_add_i32 s11, s13, 0xfffff800
	s_lshl_b64 s[0:1], s[18:19], 2
	s_add_u32 s2, s31, s0
	s_addc_u32 s3, s30, s1
	s_mov_b64 s[0:1], 0
